# dense attention loop: running max folded into the QK accumulator (q pre-scaled by 8*log2e/sqrt(d) at its e4m3 rounding, 2^-3 MFMA block scale, C = -m/8 tile), no per-score fma; all exps after QK, V fr
# speedup vs baseline: 1.0105x; 1.0105x over previous
.LBB0_385:
	s_load_dwordx2 s[18:19], s[16:17], 0xb8
	v_readlane_b32 s4, v243, 12
	s_lshl_b32 s42, s4, 2
	v_lshlrev_b32_e32 v2, 1, v1
	v_and_b32_e32 v132, 0x70, v2
	s_waitcnt lgkmcnt(0)
	s_add_u32 s27, s18, 0x14c00000
	s_addc_u32 s46, s19, 0
	s_lshl_b32 s4, s4, 7
	s_and_b32 s43, s4, 0x180
	s_add_u32 s47, s18, 0x4800000
	s_addc_u32 s48, s19, 0
	s_lshl_b32 s44, s43, 1
	s_add_u32 s49, s18, 0x3b300000
	s_addc_u32 s50, s19, 0
	v_and_b32_e32 v2, 0x1c0, v1
	s_add_i32 s5, 0, 0x10000
	v_and_b32_e32 v10, 31, v1
	v_lshl_add_u32 v135, v2, 2, s5
	v_lshrrev_b32_e32 v11, 1, v1
	s_movk_i32 s5, 0xe0
	v_and_or_b32 v2, v11, s5, v10
	v_lshlrev_b32_e32 v13, 4, v1
	v_mul_u32_u24_e32 v2, 0x2e00, v2
	v_and_b32_e32 v12, 32, v1
	v_lshrrev_b32_e32 v14, 2, v1
	v_and_b32_e32 v6, 48, v13
	v_or_b32_e32 v4, v2, v12
	v_lshlrev_b32_e32 v2, 12, v14
	v_lshlrev_b32_e32 v14, 6, v14
	v_lshrrev_b32_e32 v15, 1, v6
	v_and_b32_e32 v16, 48, v1
	v_bitop3_b32 v17, v15, v14, v16 bitop3:0xde
	v_or_b32_e32 v15, 32, v15
	v_mov_b32_e32 v3, 0
	v_bitop3_b32 v14, v15, v14, v16 bitop3:0xde
	v_lshlrev_b32_e32 v16, 3, v1
	s_movk_i32 s4, 0x70
	v_lshlrev_b32_e32 v5, 2, v1
	v_and_b32_e32 v136, 0x70, v13
	v_lshl_add_u64 v[8:9], s[18:19], 0, v[2:3]
	v_mov_b32_e32 v7, v3
	v_and_b32_e32 v138, 0xffffff80, v13
	v_xor_b32_e32 v13, v13, v1
	v_lshlrev_b32_e32 v15, 7, v10
	v_and_b32_e32 v16, 0x70, v16
	v_or_b32_e32 v19, 16, v12
	v_or_b32_e32 v21, 64, v12
	v_or_b32_e32 v22, 0x50, v12
	v_and_b32_e32 v134, 28, v5
	v_and_or_b32 v13, v13, s4, v138
	v_bitop3_b32 v18, v16, v15, v12 bitop3:0xde
	v_bitop3_b32 v20, v19, v15, v16 bitop3:0xde
	v_bitop3_b32 v21, v21, v15, v16 bitop3:0xde
	v_bitop3_b32 v15, v22, v15, v16 bitop3:0xde
	v_lshlrev_b32_e32 v16, 6, v10
	v_and_b32_e32 v5, 48, v5
	v_lshl_add_u64 v[8:9], v[8:9], 0, v[6:7]
	s_mov_b64 s[4:5], 0x3af00000
	v_or_b32_e32 v2, v6, v2
	v_cmp_ne_u32_e32 vcc, 0, v1
	v_bitop3_b32 v22, v5, v16, v12 bitop3:0xde
	v_bitop3_b32 v5, v19, v16, v5 bitop3:0xde
	v_lshl_add_u64 v[140:141], v[8:9], 0, s[4:5]
	v_lshl_add_u64 v[6:7], s[18:19], 0, v[2:3]
	s_mov_b64 s[4:5], 0x3af00100
	s_mov_b32 s21, 0
	v_cmp_eq_u32_e64 s[0:1], 0, v1
	v_mov_b32_e32 v133, v3
	v_mov_b32_e32 v139, v3
	v_mov_b32_e32 v137, v3
	v_cmp_eq_u32_e64 s[6:7], 0, v12
	v_lshl_add_u32 v184, v10, 2, v135
	v_and_b32_e32 v185, 16, v11
	v_lshl_add_u64 v[142:143], v[6:7], 0, s[4:5]
	v_add_u32_e32 v186, 0x8000, v138
	s_add_i32 s51, 0, 0x20010
	s_movk_i32 s52, 0x4000
	s_movk_i32 s53, 0x78
	s_xor_b64 s[22:23], vcc, -1
	v_mov_b32_e32 v187, 1
	s_mov_b64 s[24:25], 0x1ee02400
	s_mov_b32 s54, 0x1ee02000
	v_mov_b32_e32 v188, 0x7f7f7f7f
	s_mov_b32 s55, 0x428a7fad
	s_mov_b32 s26, 0x3e000000
	s_movk_i32 s56, 0x2000
	s_mov_b64 s[28:29], 0x80
	s_mov_b32 s57, 0x7fffe0
	s_mov_b64 s[30:31], 0x2be00200
	s_mov_b32 s58, 0xc3e00000
	s_mov_b32 s59, 0x2be00000
	s_mov_b32 s60, 0x2be01000
	s_mov_b32 s61, 0x2be02000
	s_mov_b32 s62, 0x2be05000
	s_mov_b32 s63, 0x2be06000
	s_mov_b32 s64, 0x2be07000
	s_mov_b32 s65, 0x2be0a000
	s_mov_b32 s66, 0x2be0b000
	s_mov_b32 s67, 0x2be0c000
	s_mov_b32 s68, 0x2be0f000
	s_mov_b32 s69, 0x2be10000
	s_mov_b32 s70, 0x2be11000
	v_lshlrev_b32_e32 v144, 2, v134
	v_lshlrev_b32_e32 v146, 1, v4
	v_add_u32_e32 v189, 0, v17
	v_add_u32_e32 v190, 0, v14
	v_add_u32_e32 v191, 0, v13
	v_add_u32_e32 v192, 0, v18
	v_add_u32_e32 v193, 0, v20
	v_add_u32_e32 v194, 0, v21
	v_add_u32_e32 v195, 0, v15
	v_mov_b32_e32 v196, 0xf149f2ca
	v_add_u32_e32 v197, 0, v22
	v_add_u32_e32 v198, 0, v5
	v_mov_b32_e32 v199, 0x43e00000
	s_mov_b32 s71, 0
	s_mov_b32 s72, s95
	s_branch .LBB0_387

.LBB0_408:
	s_lshr_b32 s4, s72, 3
	s_lshl_b32 s5, s72, 5
	s_bfe_u32 s10, s72, 0x20001
	s_ashr_i32 s9, s72, 8
	s_and_b32 s4, s4, 16
	s_and_b32 s11, s5, 32
	s_lshl_b32 s8, s10, 7
	s_or_b32 s4, s11, s4
	s_lshl_b32 s13, s9, 12
	s_mul_i32 s11, s9, 0x5c00000
	s_mul_hi_i32 s12, s13, 0x5c00
	s_add_u32 s11, s18, s11
	s_addc_u32 s12, s19, s12
	s_and_b32 s14, s5, 0xf00
	s_mul_i32 s5, s14, 0x5c00
	s_add_u32 s5, s11, s5
	s_addc_u32 s11, s12, 0
	s_lshl_b32 s12, s10, 9
	s_lshl_b32 s4, s4, 3
	s_or_b32 s12, s4, s12
	s_lshl_b32 s4, s12, 1
	s_add_u32 s4, s5, s4
	s_addc_u32 s5, s11, 0
	v_mov_b32_e32 v147, v3
	v_lshl_add_u64 v[8:9], s[4:5], 0, v[146:147]
	v_add_co_u32_e32 v4, vcc, s54, v8
	v_lshl_add_u64 v[32:33], v[8:9], 0, s[24:25]
	s_nop 0
	v_addc_co_u32_e32 v5, vcc, 0, v9, vcc
	global_load_dwordx4 v[4:7], v[4:5], off offset:1024
	s_nop 0
	global_load_dwordx4 v[8:11], v[32:33], off offset:16
	global_load_dwordx4 v[12:15], v[32:33], off offset:32
	global_load_dwordx4 v[16:19], v[32:33], off offset:48
	global_load_dwordx4 v[20:23], v[32:33], off offset:128
	global_load_dwordx4 v[24:27], v[32:33], off offset:160
	global_load_dwordx4 v[28:31], v[32:33], off offset:144
	s_lshl_b32 s4, s9, 2
	s_or_b32 s10, s4, s10
	s_lshl_b32 s4, s10, 12
	s_ashr_i32 s5, s4, 31
	global_load_dwordx4 v[32:35], v[32:33], off offset:176
	s_lshl_b64 s[4:5], s[4:5], 7
	s_add_u32 s4, s49, s4
	s_addc_u32 s5, s50, s5
	s_lshl_b32 s10, s10, 7
	s_ashr_i32 s11, s10, 31
	v_lshl_add_u64 v[36:37], s[4:5], 0, v[138:139]
	s_lshl_b64 s[10:11], s[10:11], 12
	v_lshl_add_u64 v[38:39], v[36:37], 0, v[136:137]
	v_lshl_add_u64 v[36:37], v[140:141], 0, s[10:11]
	global_load_dwordx4 v[40:43], v[36:37], off
	global_load_dwordx4 v[44:47], v[38:39], off
	v_mov_b32_e32 v106, v3
	v_mov_b32_e32 v100, v3
	v_mov_b32_e32 v101, v3
	v_mov_b32_e32 v107, v3
	v_mov_b32_e32 v108, v3
	v_mov_b32_e32 v109, v3
	v_mov_b32_e32 v110, v3
	v_mov_b32_e32 v111, v3
	v_mov_b32_e32 v112, v3
	v_mov_b32_e32 v113, v3
	v_mov_b32_e32 v114, v3
	v_mov_b32_e32 v102, v3
	v_mov_b32_e32 v103, v3
	v_mov_b32_e32 v104, v3
	v_mov_b32_e32 v105, v3
	s_waitcnt vmcnt(0)
	v_mov_b32_e32 v115, v3
	v_lshl_add_u64 v[148:149], s[4:5], 0, v[136:137]
	s_mov_b32 s15, 1
	v_mov_b32_e32 v145, 0
	v_mov_b32_e32 v152, v186
	s_waitcnt vmcnt(8)
	v_lshlrev_b32_e32 v51, 16, v8
	v_and_b32_e32 v8, 0xffff0000, v8
	s_waitcnt vmcnt(6)
	v_lshlrev_b32_e32 v59, 16, v16
	v_and_b32_e32 v16, 0xffff0000, v16
	v_lshlrev_b32_e32 v2, 16, v4
	v_and_b32_e32 v4, 0xffff0000, v4
	v_mul_f32_e32 v59, 0x3f8293ee, v59
	v_mul_f32_e32 v16, 0x3f8293ee, v16
	v_cvt_pk_fp8_f32 v106, v59, v16
	v_mul_f32_e32 v2, 0x3f8293ee, v2
	v_mul_f32_e32 v4, 0x3f8293ee, v4
	v_cvt_pk_fp8_f32 v100, v2, v4
	v_lshlrev_b32_e32 v60, 16, v17
	v_and_b32_e32 v2, 0xffff0000, v17
	v_lshlrev_b32_e32 v48, 16, v5
	v_and_b32_e32 v5, 0xffff0000, v5
	v_lshlrev_b32_e32 v49, 16, v6
	v_and_b32_e32 v6, 0xffff0000, v6
	v_mul_f32_e32 v60, 0x3f8293ee, v60
	v_mul_f32_e32 v2, 0x3f8293ee, v2
	v_cvt_pk_fp8_f32 v106, v60, v2 op_sel:[0,0,1]
	v_lshlrev_b32_e32 v2, 16, v18
	v_and_b32_e32 v4, 0xffff0000, v18
	v_mul_f32_e32 v49, 0x3f8293ee, v49
	v_mul_f32_e32 v6, 0x3f8293ee, v6
	v_cvt_pk_fp8_f32 v101, v49, v6
	v_mul_f32_e32 v48, 0x3f8293ee, v48
	v_mul_f32_e32 v5, 0x3f8293ee, v5
	v_cvt_pk_fp8_f32 v100, v48, v5 op_sel:[0,0,1]
	v_mul_f32_e32 v2, 0x3f8293ee, v2
	v_mul_f32_e32 v4, 0x3f8293ee, v4
	v_cvt_pk_fp8_f32 v107, v2, v4
	s_waitcnt vmcnt(5)
	v_lshlrev_b32_e32 v5, 16, v20
	v_and_b32_e32 v6, 0xffff0000, v20
	v_mul_f32_e32 v5, 0x3f8293ee, v5
	v_mul_f32_e32 v6, 0x3f8293ee, v6
	v_cvt_pk_fp8_f32 v108, v5, v6
	v_lshlrev_b32_e32 v2, 16, v19
	v_and_b32_e32 v4, 0xffff0000, v19
	v_mul_f32_e32 v2, 0x3f8293ee, v2
	v_mul_f32_e32 v4, 0x3f8293ee, v4
	v_cvt_pk_fp8_f32 v107, v2, v4 op_sel:[0,0,1]
	v_lshlrev_b32_e32 v2, 16, v21
	v_and_b32_e32 v4, 0xffff0000, v21
	v_mul_f32_e32 v2, 0x3f8293ee, v2
	v_mul_f32_e32 v4, 0x3f8293ee, v4
	v_cvt_pk_fp8_f32 v108, v2, v4 op_sel:[0,0,1]
	v_lshlrev_b32_e32 v2, 16, v22
	v_and_b32_e32 v4, 0xffff0000, v22
	v_mul_f32_e32 v2, 0x3f8293ee, v2
	v_mul_f32_e32 v4, 0x3f8293ee, v4
	v_cvt_pk_fp8_f32 v109, v2, v4
	s_waitcnt vmcnt(3)
	v_lshlrev_b32_e32 v5, 16, v28
	v_and_b32_e32 v6, 0xffff0000, v28
	v_mul_f32_e32 v5, 0x3f8293ee, v5
	v_mul_f32_e32 v6, 0x3f8293ee, v6
	v_cvt_pk_fp8_f32 v110, v5, v6
	v_lshlrev_b32_e32 v2, 16, v23
	v_and_b32_e32 v4, 0xffff0000, v23
	v_mul_f32_e32 v2, 0x3f8293ee, v2
	v_mul_f32_e32 v4, 0x3f8293ee, v4
	v_cvt_pk_fp8_f32 v109, v2, v4 op_sel:[0,0,1]
	v_lshlrev_b32_e32 v2, 16, v29
	v_and_b32_e32 v4, 0xffff0000, v29
	v_mul_f32_e32 v2, 0x3f8293ee, v2
	v_mul_f32_e32 v4, 0x3f8293ee, v4
	v_cvt_pk_fp8_f32 v110, v2, v4 op_sel:[0,0,1]
	v_lshlrev_b32_e32 v2, 16, v30
	v_and_b32_e32 v4, 0xffff0000, v30
	v_mul_f32_e32 v2, 0x3f8293ee, v2
	v_mul_f32_e32 v4, 0x3f8293ee, v4
	v_cvt_pk_fp8_f32 v111, v2, v4
	v_lshlrev_b32_e32 v5, 16, v24
	v_and_b32_e32 v6, 0xffff0000, v24
	v_mul_f32_e32 v5, 0x3f8293ee, v5
	v_mul_f32_e32 v6, 0x3f8293ee, v6
	v_cvt_pk_fp8_f32 v112, v5, v6
	v_lshlrev_b32_e32 v2, 16, v31
	v_and_b32_e32 v4, 0xffff0000, v31
	v_mul_f32_e32 v2, 0x3f8293ee, v2
	v_mul_f32_e32 v4, 0x3f8293ee, v4
	v_cvt_pk_fp8_f32 v111, v2, v4 op_sel:[0,0,1]
	v_lshlrev_b32_e32 v2, 16, v25
	v_and_b32_e32 v4, 0xffff0000, v25
	v_mul_f32_e32 v2, 0x3f8293ee, v2
	v_mul_f32_e32 v4, 0x3f8293ee, v4
	v_cvt_pk_fp8_f32 v112, v2, v4 op_sel:[0,0,1]
	v_lshlrev_b32_e32 v2, 16, v26
	v_and_b32_e32 v4, 0xffff0000, v26
	v_mul_f32_e32 v2, 0x3f8293ee, v2
	v_mul_f32_e32 v4, 0x3f8293ee, v4
	v_cvt_pk_fp8_f32 v113, v2, v4
	s_waitcnt vmcnt(2)
	v_lshlrev_b32_e32 v5, 16, v32
	v_and_b32_e32 v6, 0xffff0000, v32
	v_lshlrev_b32_e32 v53, 16, v10
	v_and_b32_e32 v10, 0xffff0000, v10
	v_mul_f32_e32 v5, 0x3f8293ee, v5
	v_mul_f32_e32 v6, 0x3f8293ee, v6
	v_cvt_pk_fp8_f32 v114, v5, v6
	v_mul_f32_e32 v51, 0x3f8293ee, v51
	v_mul_f32_e32 v8, 0x3f8293ee, v8
	v_cvt_pk_fp8_f32 v102, v51, v8
	v_mul_f32_e32 v53, 0x3f8293ee, v53
	v_mul_f32_e32 v10, 0x3f8293ee, v10
	v_cvt_pk_fp8_f32 v103, v53, v10
	v_lshlrev_b32_e32 v2, 16, v27
	v_and_b32_e32 v4, 0xffff0000, v27
	v_mul_f32_e32 v2, 0x3f8293ee, v2
	v_mul_f32_e32 v4, 0x3f8293ee, v4
	v_cvt_pk_fp8_f32 v113, v2, v4 op_sel:[0,0,1]
	v_lshlrev_b32_e32 v2, 16, v33
	v_and_b32_e32 v4, 0xffff0000, v33
	v_lshlrev_b32_e32 v50, 16, v7
	v_and_b32_e32 v7, 0xffff0000, v7
	v_lshlrev_b32_e32 v52, 16, v9
	v_and_b32_e32 v9, 0xffff0000, v9
	v_lshlrev_b32_e32 v54, 16, v11
	v_and_b32_e32 v11, 0xffff0000, v11
	v_mul_f32_e32 v2, 0x3f8293ee, v2
	v_mul_f32_e32 v4, 0x3f8293ee, v4
	v_cvt_pk_fp8_f32 v114, v2, v4 op_sel:[0,0,1]
	s_waitcnt vmcnt(1)
	v_mov_b32_e32 v4, v40
	v_mov_b32_e32 v5, v42
	v_mov_b32_e32 v42, v41
	v_lshlrev_b32_e32 v55, 16, v12
	v_and_b32_e32 v12, 0xffff0000, v12
	v_lshlrev_b32_e32 v57, 16, v14
	v_and_b32_e32 v14, 0xffff0000, v14
	v_mul_f32_e32 v50, 0x3f8293ee, v50
	v_mul_f32_e32 v7, 0x3f8293ee, v7
	v_cvt_pk_fp8_f32 v101, v50, v7 op_sel:[0,0,1]
	v_mul_f32_e32 v52, 0x3f8293ee, v52
	v_mul_f32_e32 v9, 0x3f8293ee, v9
	v_cvt_pk_fp8_f32 v102, v52, v9 op_sel:[0,0,1]
	v_mul_f32_e32 v54, 0x3f8293ee, v54
	v_mul_f32_e32 v11, 0x3f8293ee, v11
	v_cvt_pk_fp8_f32 v103, v54, v11 op_sel:[0,0,1]
	ds_write_b64 v189, v[4:5]
	ds_write_b64 v190, v[42:43]
	s_waitcnt vmcnt(0)
	ds_write_b128 v191, v[44:47] offset:32768
	s_waitcnt lgkmcnt(0)
	s_barrier
	ds_read_b128 v[40:43], v192 offset:36864
	ds_read_b128 v[4:7], v192 offset:32768
	ds_read_b128 v[44:47], v193 offset:36864
	ds_read_b128 v[8:11], v193 offset:32768
	v_mul_f32_e32 v55, 0x3f8293ee, v55
	v_mul_f32_e32 v12, 0x3f8293ee, v12
	v_cvt_pk_fp8_f32 v104, v55, v12
	v_mul_f32_e32 v57, 0x3f8293ee, v57
	v_mul_f32_e32 v14, 0x3f8293ee, v14
	v_cvt_pk_fp8_f32 v105, v57, v14
	v_lshlrev_b32_e32 v56, 16, v13
	v_and_b32_e32 v13, 0xffff0000, v13
	v_lshlrev_b32_e32 v58, 16, v15
	v_and_b32_e32 v15, 0xffff0000, v15
	v_lshlrev_b32_e32 v2, 16, v34
	v_and_b32_e32 v12, 0xffff0000, v34
	v_mul_f32_e32 v56, 0x3f8293ee, v56
	v_mul_f32_e32 v13, 0x3f8293ee, v13
	v_cvt_pk_fp8_f32 v104, v56, v13 op_sel:[0,0,1]
	v_mul_f32_e32 v58, 0x3f8293ee, v58
	v_mul_f32_e32 v15, 0x3f8293ee, v15
	v_cvt_pk_fp8_f32 v105, v58, v15 op_sel:[0,0,1]
	v_mul_f32_e32 v2, 0x3f8293ee, v2
	v_mul_f32_e32 v12, 0x3f8293ee, v12
	v_cvt_pk_fp8_f32 v115, v2, v12
	v_lshlrev_b32_e32 v2, 16, v35
	v_and_b32_e32 v56, 0xffff0000, v35
	s_waitcnt lgkmcnt(0)
	v_mfma_scale_f32_32x32x64_f8f6f4 v[20:35], v[4:11], v[100:107], 0, v188, v188 op_sel_hi:[0,0,0]
	v_mfma_scale_f32_32x32x64_f8f6f4 v[4:19], v[40:47], v[100:107], 0, v188, v188 op_sel_hi:[0,0,0]
	ds_read_b128 v[40:43], v194 offset:36864
	ds_read_b128 v[48:51], v194 offset:32768
	ds_read_b128 v[44:47], v195 offset:36864
	ds_read_b128 v[52:55], v195 offset:32768
	v_mul_f32_e32 v2, 0x3f8293ee, v2
	v_mul_f32_e32 v56, 0x3f8293ee, v56
	v_cvt_pk_fp8_f32 v115, v2, v56 op_sel:[0,0,1]
	s_waitcnt lgkmcnt(0)
	v_mfma_scale_f32_32x32x64_f8f6f4 v[20:35], v[48:55], v[108:115], v[20:35], v188, v188 op_sel_hi:[0,0,0]
	v_mfma_scale_f32_32x32x64_f8f6f4 v[4:19], v[40:47], v[108:115], v[4:19], v188, v188 op_sel_hi:[0,0,0]
	v_add_co_u32_e32 v44, vcc, s56, v38
	s_nop 15
	s_nop 15
	s_nop 0
	v_max_f32_e32 v2, v21, v21
	v_max_f32_e32 v40, v20, v20
	v_max_f32_e32 v2, v40, v2
	v_max3_f32 v2, v2, v22, v23
	v_max3_f32 v2, v2, v24, v25
	v_max3_f32 v2, v2, v26, v27
	v_max3_f32 v2, v2, v28, v29
	v_max3_f32 v2, v2, v30, v31
	v_max3_f32 v2, v2, v32, v33
	v_max3_f32 v2, v2, v34, v35
	v_max3_f32 v2, v2, v4, v5
	v_max3_f32 v2, v2, v6, v7
	v_max3_f32 v2, v2, v8, v9
	v_max3_f32 v2, v2, v10, v11
	v_max3_f32 v2, v2, v12, v13
	v_max3_f32 v2, v2, v14, v15
	v_max3_f32 v2, v2, v16, v17
	v_max3_f32 v2, v2, v18, v19
	v_mov_b32_e32 v48, v2
	s_nop 1
	v_permlane32_swap_b32_e32 v2, v48
	v_max_f32_e32 v48, v48, v48
	v_max_f32_e32 v2, v2, v2
	v_max_f32_e32 v2, v2, v48
	v_addc_co_u32_e32 v45, vcc, 0, v39, vcc
	v_add_f32_e32 v48, 0x7149f2ca, v2
	v_max_f32_e32 v2, 0xf149f2ca, v2
	v_cmp_ge_f32_e32 vcc, s55, v48
	v_sub_f32_e32 v48, 0xf149f2ca, v2
	v_mul_f32_e32 v48, 0x3e000000, v48
	v_exp_f32_e32 v48, v48
	global_load_dwordx4 v[40:43], v[36:37], off offset:64
	s_cmp_eq_u64 vcc, exec
	s_cselect_b64 vcc, -1, 0
	global_load_dwordx4 v[44:47], v[44:45], off
	v_cndmask_b32_e32 v153, v2, v196, vcc
	v_cndmask_b32_e64 v147, v48, 1.0, vcc
	v_add_co_u32_e32 v38, vcc, s52, v38
	v_mul_f32_e32 v2, 0xbe000000, v153
	s_nop 0
	v_addc_co_u32_e32 v39, vcc, 0, v39, vcc
	global_load_dwordx4 v[120:123], v[38:39], off
	global_load_dwordx4 v[116:119], v[36:37], off offset:128
	v_mov_b32_e32 v36, v2
	v_fmamk_f32 v20, v20, 0x3e000000, v2
	v_fmamk_f32 v21, v21, 0x3e000000, v2
	v_fmamk_f32 v22, v22, 0x3e000000, v2
	v_fmamk_f32 v23, v23, 0x3e000000, v2
	v_fmamk_f32 v24, v24, 0x3e000000, v2
	v_fmamk_f32 v25, v25, 0x3e000000, v2
	v_fmamk_f32 v26, v26, 0x3e000000, v2
	v_fmamk_f32 v27, v27, 0x3e000000, v2
	v_fmamk_f32 v28, v28, 0x3e000000, v2
	v_fmamk_f32 v29, v29, 0x3e000000, v2
	v_fmamk_f32 v30, v30, 0x3e000000, v2
	v_fmamk_f32 v31, v31, 0x3e000000, v2
	v_fmamk_f32 v32, v32, 0x3e000000, v2
	v_fmamk_f32 v33, v33, 0x3e000000, v2
	v_fmamk_f32 v34, v34, 0x3e000000, v2
	v_fmac_f32_e32 v36, 0x3e000000, v35
	s_lshl_b32 s4, s9, 9
	v_pk_fma_f32 v[158:159], v[16:17], s[26:27], v[2:3] op_sel_hi:[1,0,0]
	v_pk_fma_f32 v[154:155], v[4:5], s[26:27], v[2:3] op_sel_hi:[1,0,0]
	v_exp_f32_e32 v173, v20
	v_exp_f32_e32 v177, v21
	v_exp_f32_e32 v165, v22
	v_exp_f32_e32 v166, v23
	v_exp_f32_e32 v174, v24
	v_exp_f32_e32 v178, v25
	v_exp_f32_e32 v167, v26
	v_exp_f32_e32 v168, v27
	v_exp_f32_e32 v175, v28
	v_exp_f32_e32 v179, v29
	v_exp_f32_e32 v169, v30
	v_exp_f32_e32 v170, v31
	v_exp_f32_e32 v176, v32
	v_exp_f32_e32 v180, v33
	v_exp_f32_e32 v171, v34
	v_exp_f32_e32 v172, v36
	s_or_b32 s4, s4, s8
	v_mov_b32_e32 v16, v3
	v_mov_b32_e32 v17, v3
	v_pk_fma_f32 v[156:157], v[18:19], s[26:27], v[2:3] op_sel_hi:[1,0,0]
	v_pk_fma_f32 v[160:161], v[14:15], s[26:27], v[2:3] op_sel_hi:[1,0,0]
	v_pk_fma_f32 v[124:125], v[12:13], s[26:27], v[2:3] op_sel_hi:[1,0,0]
	v_pk_fma_f32 v[126:127], v[10:11], s[26:27], v[2:3] op_sel_hi:[1,0,0]
	v_pk_fma_f32 v[128:129], v[8:9], s[26:27], v[2:3] op_sel_hi:[1,0,0]
	v_pk_fma_f32 v[130:131], v[6:7], s[26:27], v[2:3] op_sel_hi:[1,0,0]
	s_waitcnt vmcnt(2)
	s_ashr_i32 s5, s4, 31
	v_mov_b32_e32 v2, v3
	v_mov_b32_e32 v6, v3
	v_mov_b32_e32 v7, v3
	v_mov_b32_e32 v8, v3
	v_mov_b32_e32 v9, v3
	v_mov_b32_e32 v10, v3
	v_mov_b32_e32 v11, v3
	v_mov_b32_e32 v12, v3
	v_mov_b32_e32 v13, v3
	v_mov_b32_e32 v14, v3
	v_mov_b32_e32 v15, v3
	s_lshl_b64 s[4:5], s[4:5], 12
	v_lshl_add_u64 v[150:151], v[142:143], 0, s[4:5]
	s_waitcnt vmcnt(3)
	v_mov_b32_e32 v4, v40
	v_mov_b32_e32 v5, v42
	v_mov_b32_e32 v42, v41
	ds_write_b64 v189, v[4:5] offset:16384
	ds_write_b64 v190, v[42:43] offset:16384
	s_waitcnt vmcnt(2)
	ds_write_b128 v191, v[44:47] offset:49152
	v_mov_b32_e32 v4, v3
	v_mov_b32_e32 v5, v3
	v_mov_b64_e32 v[66:67], v[16:17]
	v_mov_b64_e32 v[50:51], v[16:17]
	v_mov_b64_e32 v[34:35], v[16:17]
	v_mov_b64_e32 v[64:65], v[14:15]
	v_mov_b64_e32 v[62:63], v[12:13]
	v_mov_b64_e32 v[60:61], v[10:11]
	v_mov_b64_e32 v[58:59], v[8:9]
	v_mov_b64_e32 v[56:57], v[6:7]
	v_mov_b64_e32 v[54:55], v[4:5]
	v_mov_b64_e32 v[52:53], v[2:3]
	v_mov_b64_e32 v[48:49], v[14:15]
	v_mov_b64_e32 v[46:47], v[12:13]
	v_mov_b64_e32 v[44:45], v[10:11]
	v_mov_b64_e32 v[42:43], v[8:9]
	v_mov_b64_e32 v[40:41], v[6:7]
	v_mov_b64_e32 v[38:39], v[4:5]
	v_mov_b64_e32 v[36:37], v[2:3]
	v_mov_b64_e32 v[32:33], v[14:15]
	v_mov_b64_e32 v[30:31], v[12:13]
	v_mov_b64_e32 v[28:29], v[10:11]
	v_mov_b64_e32 v[26:27], v[8:9]
	v_mov_b64_e32 v[24:25], v[6:7]
	v_mov_b64_e32 v[22:23], v[4:5]
	v_mov_b64_e32 v[20:21], v[2:3]
	v_mov_b64_e32 v[18:19], v[16:17]
	v_mov_b64_e32 v[16:17], v[14:15]
	v_mov_b64_e32 v[14:15], v[12:13]
	v_mov_b64_e32 v[12:13], v[10:11]
	v_mov_b64_e32 v[10:11], v[8:9]
	v_mov_b64_e32 v[8:9], v[6:7]
	v_mov_b64_e32 v[6:7], v[4:5]
	v_mov_b64_e32 v[4:5], v[2:3]
	s_waitcnt lgkmcnt(0)
	s_barrier
	v_exp_f32_e32 v154, v154
	v_exp_f32_e32 v155, v155
	v_exp_f32_e32 v130, v130
	v_exp_f32_e32 v131, v131
	v_exp_f32_e32 v128, v128
	v_exp_f32_e32 v129, v129
	v_exp_f32_e32 v126, v126
	v_exp_f32_e32 v127, v127
	v_exp_f32_e32 v124, v124
	v_exp_f32_e32 v125, v125
	v_exp_f32_e32 v160, v160
	v_exp_f32_e32 v161, v161
	v_exp_f32_e32 v158, v158
	v_exp_f32_e32 v159, v159
	v_exp_f32_e32 v156, v156
	v_exp_f32_e32 v157, v157
	v_mul_f32_e32 v216, 0xbe000000, v153
	v_mov_b32_e32 v217, v216
	v_mov_b32_e32 v218, v216
	v_mov_b32_e32 v219, v216
	v_mov_b32_e32 v220, v216
	v_mov_b32_e32 v221, v216
	v_mov_b32_e32 v222, v216
	v_mov_b32_e32 v223, v216
	v_mov_b32_e32 v224, v216
	v_mov_b32_e32 v225, v216
	v_mov_b32_e32 v226, v216
	v_mov_b32_e32 v227, v216
	v_mov_b32_e32 v228, v216
	v_mov_b32_e32 v229, v216
	v_mov_b32_e32 v230, v216
	v_mov_b32_e32 v231, v216
	v_mov_b32_e32 v247, 0x7c7c7c7c
.LBB0_409:
	s_waitcnt vmcnt(0)
	v_mov_b32_e32 v254, v116
	v_mov_b32_e32 v255, v118
	ds_write_b64 v189, v[254:255] offset:8192
	v_mov_b32_e32 v244, v117
	v_mov_b32_e32 v245, v119
	ds_write_b64 v190, v[244:245] offset:8192
	ds_write_b128 v191, v[120:123] offset:40960
	ds_read_b128 v[200:203], v192 offset:53248
	ds_read_b128 v[68:71], v192 offset:49152
	ds_read_b128 v[72:75], v193 offset:49152
	ds_read_b128 v[204:207], v193 offset:53248
	v_add_u32_e32 v252, 0xffffe000, v152
	v_mov_b32_e32 v253, v3
	v_lshl_add_u64 v[252:253], v[148:149], 0, v[252:253]
	v_cvt_pk_fp8_f32 v232, v173, v177
	v_cvt_pk_fp8_f32 v233, v174, v178
	v_cvt_pk_fp8_f32 v234, v175, v179
	v_cvt_pk_fp8_f32 v235, v176, v180
	v_cvt_pk_fp8_f32 v232, v165, v166 op_sel:[0,0,1]
	v_cvt_pk_fp8_f32 v233, v167, v168 op_sel:[0,0,1]
	v_cvt_pk_fp8_f32 v234, v169, v170 op_sel:[0,0,1]
	v_cvt_pk_fp8_f32 v235, v171, v172 op_sel:[0,0,1]
	v_cvt_pk_fp8_f32 v236, v154, v155
	s_waitcnt lgkmcnt(1)
	v_mfma_scale_f32_32x32x64_f8f6f4 v[84:99], v[68:75], v[100:107], v[216:231], v188, v247 op_sel_hi:[0,0,0]
	v_cvt_pk_fp8_f32 v237, v128, v129
	v_cvt_pk_fp8_f32 v238, v124, v125
	v_cvt_pk_fp8_f32 v239, v158, v159
	v_cvt_pk_fp8_f32 v236, v130, v131 op_sel:[0,0,1]
	v_cvt_pk_fp8_f32 v237, v126, v127 op_sel:[0,0,1]
	v_cvt_pk_fp8_f32 v238, v160, v161 op_sel:[0,0,1]
	v_cvt_pk_fp8_f32 v239, v156, v157 op_sel:[0,0,1]
	v_add_f32_e32 v241, v128, v129
	v_add_f32_e32 v240, v173, v177
	v_add_f32_e32 v241, v124, v241
	v_add_f32_e32 v240, v165, v240
	v_add_f32_e32 v241, v125, v241
	s_waitcnt lgkmcnt(0)
	v_mfma_scale_f32_32x32x64_f8f6f4 v[68:83], v[200:207], v[100:107], v[216:231], v188, v247 op_sel_hi:[0,0,0]
	ds_read_b128 v[200:203], v194 offset:53248
	ds_read_b128 v[208:211], v194 offset:49152
	ds_read_b128 v[212:215], v195 offset:49152
	ds_read_b128 v[204:207], v195 offset:53248
	v_add_f32_e32 v240, v166, v240
	v_add_f32_e32 v241, v126, v241
	v_add_f32_e32 v240, v174, v240
	v_add_f32_e32 v241, v127, v241
	v_add_f32_e32 v240, v178, v240
	v_add_f32_e32 v241, v130, v241
	v_add_f32_e32 v240, v167, v240
	v_add_f32_e32 v241, v131, v241
	v_add_f32_e32 v240, v168, v240
	v_add_f32_e32 v241, v154, v241
	v_add_f32_e32 v240, v175, v240
	v_add_f32_e32 v241, v155, v241
	s_waitcnt lgkmcnt(1)
	v_mfma_scale_f32_32x32x64_f8f6f4 v[84:99], v[208:215], v[108:115], v[84:99], v188, v247 op_sel_hi:[0,0,0]
	v_add_f32_e32 v240, v179, v240
	v_add_f32_e32 v241, v160, v241
	v_add_f32_e32 v240, v169, v240
	v_add_f32_e32 v241, v161, v241
	v_add_f32_e32 v240, v170, v240
	v_add_f32_e32 v241, v158, v241
	v_add_f32_e32 v240, v176, v240
	v_add_f32_e32 v241, v159, v241
	v_add_f32_e32 v240, v180, v240
	v_add_f32_e32 v241, v156, v241
	v_add_f32_e32 v240, v171, v240
	v_add_f32_e32 v241, v157, v241
	s_waitcnt lgkmcnt(0)
	v_mfma_scale_f32_32x32x64_f8f6f4 v[68:83], v[200:207], v[108:115], v[68:83], v188, v247 op_sel_hi:[0,0,0]
	ds_read_b128 v[200:203], v197
	ds_read_b128 v[204:207], v198
	ds_read_b128 v[208:211], v197 offset:2048
	ds_read_b128 v[212:215], v198 offset:2048
	global_load_dwordx4 v[124:127], v[150:151], off offset:-64
	global_load_dwordx4 v[128:131], v[252:253], off
	v_add_f32_e32 v240, v172, v240
	v_add_f32_e32 v162, v240, v241
	v_mov_b32_e32 v163, v162
	s_nop 0
	s_nop 0
	v_permlane32_swap_b32_e32 v162, v163
	v_max3_f32 v246, v84, v85, v86
	v_max3_f32 v246, v246, v87, v88
	v_max3_f32 v246, v246, v89, v90
	v_max3_f32 v246, v246, v91, v92
	v_max3_f32 v246, v246, v93, v94
	v_max3_f32 v246, v246, v95, v96
	v_max3_f32 v246, v246, v97, v98
	v_max_f32_e32 v246, v246, v99
	v_max3_f32 v248, v68, v69, v70
	s_waitcnt lgkmcnt(2)
	v_mfma_scale_f32_32x32x64_f8f6f4 v[52:67], v[232:239], v[200:207], v[52:67], v188, v188 op_sel_hi:[0,0,0]
	v_max3_f32 v248, v248, v71, v72
	v_max3_f32 v248, v248, v73, v74
	v_max3_f32 v248, v248, v75, v76
	v_max3_f32 v248, v248, v77, v78
	v_max3_f32 v248, v248, v79, v80
	v_max3_f32 v248, v248, v81, v82
	v_max_f32_e32 v248, v248, v83
	v_max_f32_e32 v250, v246, v248
	v_mov_b32_e32 v251, v250
	s_nop 0
	s_nop 0
	v_permlane32_swap_b32_e32 v250, v251
	v_max_f32_e32 v250, v250, v251
	v_cmp_ge_f32_e32 vcc, 0x410a7fad, v250
	s_cmp_eq_u64 vcc, exec
	s_waitcnt lgkmcnt(0)
	v_mfma_scale_f32_32x32x64_f8f6f4 v[36:51], v[232:239], v[208:215], v[36:51], v188, v188 op_sel_hi:[0,0,0]
	ds_read_b128 v[200:203], v197 offset:4096
	ds_read_b128 v[204:207], v198 offset:4096
	ds_read_b128 v[208:211], v197 offset:6144
	ds_read_b128 v[212:215], v198 offset:6144
	s_cselect_b64 s[4:5], -1, 0
	v_max_f32_e32 v250, 0, v250
	v_exp_f32_e64 v155, -v250
	v_fmamk_f32 v2, v250, 0x41000000, v153
	v_cndmask_b32_e64 v164, v155, 1.0, s[4:5]
	v_cndmask_b32_e64 v154, v2, v153, s[4:5]
	v_exp_f32_e32 v165, v84
	v_exp_f32_e32 v169, v85
	v_exp_f32_e32 v2, v86
	v_exp_f32_e32 v155, v87
	v_exp_f32_e32 v166, v88
	v_exp_f32_e32 v170, v89
	v_exp_f32_e32 v156, v90
	s_waitcnt lgkmcnt(2)
	v_mfma_scale_f32_32x32x64_f8f6f4 v[20:35], v[232:239], v[200:207], v[20:35], v188, v188 op_sel_hi:[0,0,0]
	v_exp_f32_e32 v157, v91
	v_exp_f32_e32 v167, v92
	v_exp_f32_e32 v171, v93
	v_exp_f32_e32 v158, v94
	v_exp_f32_e32 v159, v95
	v_exp_f32_e32 v168, v96
	v_exp_f32_e32 v172, v97
	v_exp_f32_e32 v160, v98
	v_exp_f32_e32 v161, v99
	v_exp_f32_e32 v173, v68
	v_exp_f32_e32 v174, v69
	v_exp_f32_e32 v175, v70
	v_exp_f32_e32 v176, v71
	s_waitcnt lgkmcnt(0)
	v_mfma_scale_f32_32x32x64_f8f6f4 v[4:19], v[232:239], v[208:215], v[4:19], v188, v188 op_sel_hi:[0,0,0]
	v_exp_f32_e32 v177, v72
	v_exp_f32_e32 v178, v73
	v_exp_f32_e32 v179, v74
	v_exp_f32_e32 v180, v75
	v_exp_f32_e32 v181, v76
	v_exp_f32_e32 v182, v77
	v_exp_f32_e32 v183, v78
	v_exp_f32_e32 v246, v79
	v_exp_f32_e32 v248, v80
	v_exp_f32_e32 v250, v81
	v_exp_f32_e32 v251, v82
	v_exp_f32_e32 v153, v83
	s_cmp_eq_u64 s[4:5], 0
	s_cbranch_scc0 .Lring_noresc_a0
	s_nop 15
	s_nop 7
	s_and_saveexec_b64 s[8:9], s[6:7]
	ds_write_b32 v184, v164 offset:128
	s_or_b64 exec, exec, s[8:9]
	s_waitcnt lgkmcnt(0)
	v_add_u32_e32 v252, v135, v185
	ds_read_b128 v[212:215], v252 offset:224
	ds_read_b128 v[208:211], v252 offset:192
	ds_read_b128 v[204:207], v252 offset:160
	ds_read_b128 v[200:203], v252 offset:128
	v_mul_f32_e32 v165, v165, v164
	v_mul_f32_e32 v169, v169, v164
	v_mul_f32_e32 v2, v2, v164
	v_mul_f32_e32 v155, v155, v164
	v_mul_f32_e32 v166, v166, v164
	v_mul_f32_e32 v170, v170, v164
	v_mul_f32_e32 v156, v156, v164
	v_mul_f32_e32 v157, v157, v164
	v_mul_f32_e32 v167, v167, v164
	v_mul_f32_e32 v171, v171, v164
	v_mul_f32_e32 v158, v158, v164
	v_mul_f32_e32 v159, v159, v164
	v_mul_f32_e32 v168, v168, v164
	v_mul_f32_e32 v172, v172, v164
	v_mul_f32_e32 v160, v160, v164
	v_mul_f32_e32 v161, v161, v164
	v_mul_f32_e32 v173, v173, v164
	v_mul_f32_e32 v174, v174, v164
	v_mul_f32_e32 v175, v175, v164
	v_mul_f32_e32 v176, v176, v164
	v_mul_f32_e32 v177, v177, v164
	v_mul_f32_e32 v178, v178, v164
	v_mul_f32_e32 v179, v179, v164
	v_mul_f32_e32 v180, v180, v164
	v_mul_f32_e32 v181, v181, v164
	v_mul_f32_e32 v182, v182, v164
	v_mul_f32_e32 v183, v183, v164
	v_mul_f32_e32 v246, v246, v164
	v_mul_f32_e32 v248, v248, v164
	v_mul_f32_e32 v250, v250, v164
	v_mul_f32_e32 v251, v251, v164
	v_mul_f32_e32 v153, v153, v164
	v_mul_f32_e32 v216, 0xbe000000, v154
	v_mov_b32_e32 v217, v216
	v_mov_b32_e32 v218, v216
	v_mov_b32_e32 v219, v216
	v_mov_b32_e32 v220, v216
	v_mov_b32_e32 v221, v216
	v_mov_b32_e32 v222, v216
	v_mov_b32_e32 v223, v216
	v_mov_b32_e32 v224, v216
	v_mov_b32_e32 v225, v216
	v_mov_b32_e32 v226, v216
	v_mov_b32_e32 v227, v216
	v_mov_b32_e32 v228, v216
	v_mov_b32_e32 v229, v216
	v_mov_b32_e32 v230, v216
	v_mov_b32_e32 v231, v216
	s_waitcnt lgkmcnt(0)
	v_pk_mul_f32 v[52:53], v[52:53], v[200:201]
	v_pk_mul_f32 v[54:55], v[54:55], v[202:203]
	v_pk_mul_f32 v[56:57], v[56:57], v[204:205]
	v_pk_mul_f32 v[58:59], v[58:59], v[206:207]
	v_pk_mul_f32 v[60:61], v[60:61], v[208:209]
	v_pk_mul_f32 v[62:63], v[62:63], v[210:211]
	v_pk_mul_f32 v[64:65], v[64:65], v[212:213]
	v_pk_mul_f32 v[66:67], v[66:67], v[214:215]
	v_pk_mul_f32 v[36:37], v[36:37], v[200:201]
	v_pk_mul_f32 v[38:39], v[38:39], v[202:203]
	v_pk_mul_f32 v[40:41], v[40:41], v[204:205]
	v_pk_mul_f32 v[42:43], v[42:43], v[206:207]
	v_pk_mul_f32 v[44:45], v[44:45], v[208:209]
	v_pk_mul_f32 v[46:47], v[46:47], v[210:211]
	v_pk_mul_f32 v[48:49], v[48:49], v[212:213]
	v_pk_mul_f32 v[50:51], v[50:51], v[214:215]
	v_pk_mul_f32 v[20:21], v[20:21], v[200:201]
	v_pk_mul_f32 v[22:23], v[22:23], v[202:203]
	v_pk_mul_f32 v[24:25], v[24:25], v[204:205]
	v_pk_mul_f32 v[26:27], v[26:27], v[206:207]
	v_pk_mul_f32 v[28:29], v[28:29], v[208:209]
	v_pk_mul_f32 v[30:31], v[30:31], v[210:211]
	v_pk_mul_f32 v[32:33], v[32:33], v[212:213]
	v_pk_mul_f32 v[34:35], v[34:35], v[214:215]
	v_pk_mul_f32 v[4:5], v[4:5], v[200:201]
	v_pk_mul_f32 v[6:7], v[6:7], v[202:203]
	v_pk_mul_f32 v[8:9], v[8:9], v[204:205]
	v_pk_mul_f32 v[10:11], v[10:11], v[206:207]
	v_pk_mul_f32 v[12:13], v[12:13], v[208:209]
	v_pk_mul_f32 v[14:15], v[14:15], v[210:211]
	v_pk_mul_f32 v[16:17], v[16:17], v[212:213]
	v_pk_mul_f32 v[18:19], v[18:19], v[214:215]

.Lring_noload_b0:
	ds_read_b128 v[200:203], v192 offset:45056
	ds_read_b128 v[68:71], v192 offset:40960
	ds_read_b128 v[72:75], v193 offset:40960
	ds_read_b128 v[204:207], v193 offset:45056
	v_cvt_pk_fp8_f32 v232, v165, v169
	v_cvt_pk_fp8_f32 v233, v166, v170
	v_cvt_pk_fp8_f32 v234, v167, v171
	v_cvt_pk_fp8_f32 v235, v168, v172
	v_cvt_pk_fp8_f32 v232, v2, v155 op_sel:[0,0,1]
	v_cvt_pk_fp8_f32 v233, v156, v157 op_sel:[0,0,1]
	v_cvt_pk_fp8_f32 v234, v158, v159 op_sel:[0,0,1]
	v_cvt_pk_fp8_f32 v235, v160, v161 op_sel:[0,0,1]
	v_cvt_pk_fp8_f32 v236, v173, v174
	v_cvt_pk_fp8_f32 v237, v177, v178
	v_cvt_pk_fp8_f32 v238, v181, v182
	v_cvt_pk_fp8_f32 v239, v248, v250
	s_waitcnt lgkmcnt(1)
	v_mfma_scale_f32_32x32x64_f8f6f4 v[84:99], v[68:75], v[100:107], v[216:231], v188, v247 op_sel_hi:[0,0,0]
	v_cvt_pk_fp8_f32 v236, v175, v176 op_sel:[0,0,1]
	v_cvt_pk_fp8_f32 v237, v179, v180 op_sel:[0,0,1]
	v_cvt_pk_fp8_f32 v238, v183, v246 op_sel:[0,0,1]
	v_cvt_pk_fp8_f32 v239, v251, v153 op_sel:[0,0,1]
	v_add_f32_e32 v241, v246, v248
	v_add_f32_e32 v240, v165, v169
	v_add_f32_e32 v241, v250, v241
	v_add_f32_e32 v240, v2, v240
	v_add_f32_e32 v241, v251, v241
	v_add_f32_e32 v240, v155, v240
	v_add_f32_e32 v241, v173, v241
	v_add_f32_e32 v240, v166, v240
	s_waitcnt lgkmcnt(0)
	v_mfma_scale_f32_32x32x64_f8f6f4 v[68:83], v[200:207], v[100:107], v[216:231], v188, v247 op_sel_hi:[0,0,0]
	ds_read_b128 v[200:203], v194 offset:45056
	ds_read_b128 v[208:211], v194 offset:40960
	ds_read_b128 v[212:215], v195 offset:40960
	ds_read_b128 v[204:207], v195 offset:45056
	v_add_f32_e32 v241, v174, v241
	v_add_f32_e32 v240, v170, v240
	v_add_f32_e32 v241, v175, v241
	v_add_f32_e32 v240, v156, v240
	v_add_f32_e32 v241, v176, v241
	v_add_f32_e32 v240, v157, v240
	v_add_f32_e32 v241, v177, v241
	v_add_f32_e32 v240, v167, v240
	v_add_f32_e32 v241, v178, v241
	v_add_f32_e32 v240, v171, v240
	v_add_f32_e32 v241, v179, v241
	v_add_f32_e32 v240, v158, v240
	s_waitcnt lgkmcnt(1)
	v_mfma_scale_f32_32x32x64_f8f6f4 v[84:99], v[208:215], v[108:115], v[84:99], v188, v247 op_sel_hi:[0,0,0]
	v_add_f32_e32 v241, v180, v241
	v_add_f32_e32 v240, v159, v240
	v_add_f32_e32 v241, v181, v241
	v_add_f32_e32 v240, v168, v240
	v_add_f32_e32 v241, v182, v241
	v_add_f32_e32 v240, v172, v240
	v_add_f32_e32 v241, v183, v241
	v_add_f32_e32 v240, v160, v240
	v_add_f32_e32 v241, v153, v241
	v_add_f32_e32 v240, v161, v240
	v_add_f32_e32 v181, v240, v241
	v_mov_b32_e32 v182, v181
	s_nop 0
	s_nop 0
	v_permlane32_swap_b32_e32 v181, v182
	s_waitcnt lgkmcnt(0)
	v_mfma_scale_f32_32x32x64_f8f6f4 v[68:83], v[200:207], v[108:115], v[68:83], v188, v247 op_sel_hi:[0,0,0]
	ds_read_b128 v[200:203], v197 offset:16384
	ds_read_b128 v[204:207], v198 offset:16384
	ds_read_b128 v[208:211], v197 offset:18432
	ds_read_b128 v[212:215], v198 offset:18432
	v_max3_f32 v246, v84, v85, v86
	v_max3_f32 v246, v246, v87, v88
	v_max3_f32 v246, v246, v89, v90
	v_max3_f32 v246, v246, v91, v92
	v_max3_f32 v246, v246, v93, v94
	v_max3_f32 v246, v246, v95, v96
	v_max3_f32 v246, v246, v97, v98
	v_max_f32_e32 v246, v246, v99
	s_nop 7
	v_max3_f32 v248, v68, v69, v70
	v_max3_f32 v248, v248, v71, v72
	v_max3_f32 v248, v248, v73, v74
	v_max3_f32 v248, v248, v75, v76
	v_max3_f32 v248, v248, v77, v78
	s_waitcnt lgkmcnt(2)
	v_mfma_scale_f32_32x32x64_f8f6f4 v[52:67], v[232:239], v[200:207], v[52:67], v188, v188 op_sel_hi:[0,0,0]
	v_max3_f32 v248, v248, v79, v80
	v_max3_f32 v248, v248, v81, v82
	v_max_f32_e32 v248, v248, v83
	v_max_f32_e32 v250, v246, v248
	v_mov_b32_e32 v251, v250
	s_nop 0
	s_nop 0
	v_permlane32_swap_b32_e32 v250, v251
	v_max_f32_e32 v250, v250, v251
	v_cmp_ge_f32_e32 vcc, 0x410a7fad, v250
	s_cmp_eq_u64 vcc, exec
	s_cselect_b64 s[4:5], -1, 0
	v_max_f32_e32 v250, 0, v250
	v_exp_f32_e64 v2, -v250
	v_fmamk_f32 v153, v250, 0x41000000, v154
	s_waitcnt lgkmcnt(0)
	v_mfma_scale_f32_32x32x64_f8f6f4 v[36:51], v[232:239], v[208:215], v[36:51], v188, v188 op_sel_hi:[0,0,0]
	ds_read_b128 v[200:203], v197 offset:20480
	ds_read_b128 v[204:207], v198 offset:20480
	ds_read_b128 v[208:211], v197 offset:22528
	ds_read_b128 v[212:215], v198 offset:22528
	v_cndmask_b32_e64 v2, v2, 1.0, s[4:5]
	v_cndmask_b32_e64 v153, v153, v154, s[4:5]
	v_exp_f32_e32 v173, v84
	v_exp_f32_e32 v177, v85
	v_exp_f32_e32 v165, v86
	v_exp_f32_e32 v166, v87
	v_exp_f32_e32 v174, v88
	v_exp_f32_e32 v178, v89
	v_exp_f32_e32 v167, v90
	v_exp_f32_e32 v168, v91
	v_exp_f32_e32 v175, v92
	v_exp_f32_e32 v179, v93
	v_exp_f32_e32 v169, v94
	s_waitcnt lgkmcnt(2)
	v_mfma_scale_f32_32x32x64_f8f6f4 v[20:35], v[232:239], v[200:207], v[20:35], v188, v188 op_sel_hi:[0,0,0]
	v_exp_f32_e32 v170, v95
	v_exp_f32_e32 v176, v96
	v_exp_f32_e32 v180, v97
	v_exp_f32_e32 v171, v98
	v_exp_f32_e32 v172, v99
	v_exp_f32_e32 v154, v68
	v_exp_f32_e32 v155, v69
	v_exp_f32_e32 v130, v70
	v_exp_f32_e32 v131, v71
	v_exp_f32_e32 v128, v72
	v_exp_f32_e32 v129, v73
	v_exp_f32_e32 v126, v74
	v_exp_f32_e32 v127, v75
	s_waitcnt lgkmcnt(0)
	v_mfma_scale_f32_32x32x64_f8f6f4 v[4:19], v[232:239], v[208:215], v[4:19], v188, v188 op_sel_hi:[0,0,0]
	v_exp_f32_e32 v124, v76
	v_exp_f32_e32 v125, v77
	v_exp_f32_e32 v160, v78
	v_exp_f32_e32 v161, v79
	v_exp_f32_e32 v158, v80
	v_exp_f32_e32 v159, v81
	v_exp_f32_e32 v156, v82
	v_exp_f32_e32 v157, v83
	v_add_f32_e32 v249, v162, v163
	v_fmac_f32_e32 v249, v147, v145
	v_add_f32_e32 v145, v181, v182
	v_fmac_f32_e32 v145, v249, v164
	s_cmp_eq_u64 s[4:5], 0
	s_cbranch_scc0 .Lring_noresc_b0
	s_nop 15
	s_nop 7
	s_and_saveexec_b64 s[10:11], s[6:7]
	ds_write_b32 v184, v2 offset:128
	s_or_b64 exec, exec, s[10:11]
	s_waitcnt lgkmcnt(0)
	v_add_u32_e32 v252, v135, v185
	ds_read_b128 v[212:215], v252 offset:224
	ds_read_b128 v[208:211], v252 offset:192
	ds_read_b128 v[204:207], v252 offset:160
	ds_read_b128 v[200:203], v252 offset:128
	v_mul_f32_e32 v173, v173, v2
	v_mul_f32_e32 v177, v177, v2
	v_mul_f32_e32 v165, v165, v2
	v_mul_f32_e32 v166, v166, v2
	v_mul_f32_e32 v174, v174, v2
	v_mul_f32_e32 v178, v178, v2
	v_mul_f32_e32 v167, v167, v2
	v_mul_f32_e32 v168, v168, v2
	v_mul_f32_e32 v175, v175, v2
	v_mul_f32_e32 v179, v179, v2
	v_mul_f32_e32 v169, v169, v2
	v_mul_f32_e32 v170, v170, v2
	v_mul_f32_e32 v176, v176, v2
	v_mul_f32_e32 v180, v180, v2
	v_mul_f32_e32 v171, v171, v2
	v_mul_f32_e32 v172, v172, v2
	v_mul_f32_e32 v154, v154, v2
	v_mul_f32_e32 v155, v155, v2
	v_mul_f32_e32 v130, v130, v2
	v_mul_f32_e32 v131, v131, v2
	v_mul_f32_e32 v128, v128, v2
	v_mul_f32_e32 v129, v129, v2
	v_mul_f32_e32 v126, v126, v2
	v_mul_f32_e32 v127, v127, v2
	v_mul_f32_e32 v124, v124, v2
	v_mul_f32_e32 v125, v125, v2
	v_mul_f32_e32 v160, v160, v2
	v_mul_f32_e32 v161, v161, v2
	v_mul_f32_e32 v158, v158, v2
	v_mul_f32_e32 v159, v159, v2
	v_mul_f32_e32 v156, v156, v2
	v_mul_f32_e32 v157, v157, v2
	v_mul_f32_e32 v216, 0xbe000000, v153
	v_mov_b32_e32 v217, v216
	v_mov_b32_e32 v218, v216
	v_mov_b32_e32 v219, v216
	v_mov_b32_e32 v220, v216
	v_mov_b32_e32 v221, v216
	v_mov_b32_e32 v222, v216
	v_mov_b32_e32 v223, v216
	v_mov_b32_e32 v224, v216
	v_mov_b32_e32 v225, v216
	v_mov_b32_e32 v226, v216
	v_mov_b32_e32 v227, v216
	v_mov_b32_e32 v228, v216
	v_mov_b32_e32 v229, v216
	v_mov_b32_e32 v230, v216
	v_mov_b32_e32 v231, v216
	s_waitcnt lgkmcnt(0)
	v_pk_mul_f32 v[52:53], v[52:53], v[200:201]
	v_pk_mul_f32 v[54:55], v[54:55], v[202:203]
	v_pk_mul_f32 v[56:57], v[56:57], v[204:205]
	v_pk_mul_f32 v[58:59], v[58:59], v[206:207]
	v_pk_mul_f32 v[60:61], v[60:61], v[208:209]
	v_pk_mul_f32 v[62:63], v[62:63], v[210:211]
	v_pk_mul_f32 v[64:65], v[64:65], v[212:213]
	v_pk_mul_f32 v[66:67], v[66:67], v[214:215]
	v_pk_mul_f32 v[36:37], v[36:37], v[200:201]
	v_pk_mul_f32 v[38:39], v[38:39], v[202:203]
	v_pk_mul_f32 v[40:41], v[40:41], v[204:205]
	v_pk_mul_f32 v[42:43], v[42:43], v[206:207]
	v_pk_mul_f32 v[44:45], v[44:45], v[208:209]
	v_pk_mul_f32 v[46:47], v[46:47], v[210:211]
	v_pk_mul_f32 v[48:49], v[48:49], v[212:213]
	v_pk_mul_f32 v[50:51], v[50:51], v[214:215]
	v_pk_mul_f32 v[20:21], v[20:21], v[200:201]
	v_pk_mul_f32 v[22:23], v[22:23], v[202:203]
	v_pk_mul_f32 v[24:25], v[24:25], v[204:205]
	v_pk_mul_f32 v[26:27], v[26:27], v[206:207]
	v_pk_mul_f32 v[28:29], v[28:29], v[208:209]
	v_pk_mul_f32 v[30:31], v[30:31], v[210:211]
	v_pk_mul_f32 v[32:33], v[32:33], v[212:213]
	v_pk_mul_f32 v[34:35], v[34:35], v[214:215]
	v_pk_mul_f32 v[4:5], v[4:5], v[200:201]
	v_pk_mul_f32 v[6:7], v[6:7], v[202:203]
	v_pk_mul_f32 v[8:9], v[8:9], v[204:205]
	v_pk_mul_f32 v[10:11], v[10:11], v[206:207]
	v_pk_mul_f32 v[12:13], v[12:13], v[208:209]
	v_pk_mul_f32 v[14:15], v[14:15], v[210:211]
	v_pk_mul_f32 v[16:17], v[16:17], v[212:213]
	v_pk_mul_f32 v[18:19], v[18:19], v[214:215]
.Lring_noresc_b0:
	s_add_i32 s15, s15, 2
	v_lshl_add_u64 v[150:151], v[150:151], 0, s[28:29]
	v_add_u32_e32 v152, 0x4000, v152
	s_and_b64 vcc, exec, s[8:9]
	s_waitcnt lgkmcnt(0)
	s_barrier
	s_cbranch_vccnz .LBB0_421
	v_mov_b32_e32 v147, v2
	s_waitcnt vmcnt(0)
	v_mov_b32_e32 v254, v116
	v_mov_b32_e32 v255, v118
	ds_write_b64 v189, v[254:255]
	v_mov_b32_e32 v244, v117
	v_mov_b32_e32 v245, v119
	ds_write_b64 v190, v[244:245]
	ds_write_b128 v191, v[120:123] offset:32768
	ds_read_b128 v[200:203], v192 offset:61440
	ds_read_b128 v[68:71], v192 offset:57344
	ds_read_b128 v[72:75], v193 offset:57344
	ds_read_b128 v[204:207], v193 offset:61440
	v_add_u32_e32 v252, 0xffffe000, v152
	v_mov_b32_e32 v253, v3
	v_lshl_add_u64 v[252:253], v[148:149], 0, v[252:253]
	v_cvt_pk_fp8_f32 v232, v173, v177
	v_cvt_pk_fp8_f32 v233, v174, v178
	v_cvt_pk_fp8_f32 v234, v175, v179
	v_cvt_pk_fp8_f32 v235, v176, v180
	v_cvt_pk_fp8_f32 v232, v165, v166 op_sel:[0,0,1]
	v_cvt_pk_fp8_f32 v233, v167, v168 op_sel:[0,0,1]
	v_cvt_pk_fp8_f32 v234, v169, v170 op_sel:[0,0,1]
	v_cvt_pk_fp8_f32 v235, v171, v172 op_sel:[0,0,1]
	v_cvt_pk_fp8_f32 v236, v154, v155
	s_waitcnt lgkmcnt(1)
	v_mfma_scale_f32_32x32x64_f8f6f4 v[84:99], v[68:75], v[100:107], v[216:231], v188, v247 op_sel_hi:[0,0,0]
	v_cvt_pk_fp8_f32 v237, v128, v129
	v_cvt_pk_fp8_f32 v238, v124, v125
	v_cvt_pk_fp8_f32 v239, v158, v159
	v_cvt_pk_fp8_f32 v236, v130, v131 op_sel:[0,0,1]
	v_cvt_pk_fp8_f32 v237, v126, v127 op_sel:[0,0,1]
	v_cvt_pk_fp8_f32 v238, v160, v161 op_sel:[0,0,1]
	v_cvt_pk_fp8_f32 v239, v156, v157 op_sel:[0,0,1]
	v_add_f32_e32 v241, v128, v129
	v_add_f32_e32 v240, v173, v177
	v_add_f32_e32 v241, v124, v241
	v_add_f32_e32 v240, v165, v240
	v_add_f32_e32 v241, v125, v241
	s_waitcnt lgkmcnt(0)
	v_mfma_scale_f32_32x32x64_f8f6f4 v[68:83], v[200:207], v[100:107], v[216:231], v188, v247 op_sel_hi:[0,0,0]
	ds_read_b128 v[200:203], v194 offset:61440
	ds_read_b128 v[208:211], v194 offset:57344
	ds_read_b128 v[212:215], v195 offset:57344
	ds_read_b128 v[204:207], v195 offset:61440
	v_add_f32_e32 v240, v166, v240
	v_add_f32_e32 v241, v126, v241
	v_add_f32_e32 v240, v174, v240
	v_add_f32_e32 v241, v127, v241
	v_add_f32_e32 v240, v178, v240
	v_add_f32_e32 v241, v130, v241
	v_add_f32_e32 v240, v167, v240
	v_add_f32_e32 v241, v131, v241
	v_add_f32_e32 v240, v168, v240
	v_add_f32_e32 v241, v154, v241
	v_add_f32_e32 v240, v175, v240
	v_add_f32_e32 v241, v155, v241
	s_waitcnt lgkmcnt(1)
	v_mfma_scale_f32_32x32x64_f8f6f4 v[84:99], v[208:215], v[108:115], v[84:99], v188, v247 op_sel_hi:[0,0,0]
	v_add_f32_e32 v240, v179, v240
	v_add_f32_e32 v241, v160, v241
	v_add_f32_e32 v240, v169, v240
	v_add_f32_e32 v241, v161, v241
	v_add_f32_e32 v240, v170, v240
	v_add_f32_e32 v241, v158, v241
	v_add_f32_e32 v240, v176, v240
	v_add_f32_e32 v241, v159, v241
	v_add_f32_e32 v240, v180, v240
	v_add_f32_e32 v241, v156, v241
	v_add_f32_e32 v240, v171, v240
	v_add_f32_e32 v241, v157, v241
	s_waitcnt lgkmcnt(0)
	v_mfma_scale_f32_32x32x64_f8f6f4 v[68:83], v[200:207], v[108:115], v[68:83], v188, v247 op_sel_hi:[0,0,0]
	ds_read_b128 v[200:203], v197 offset:8192
	ds_read_b128 v[204:207], v198 offset:8192
	ds_read_b128 v[208:211], v197 offset:10240
	ds_read_b128 v[212:215], v198 offset:10240
	global_load_dwordx4 v[124:127], v[150:151], off offset:-64
	global_load_dwordx4 v[128:131], v[252:253], off
	v_add_f32_e32 v240, v172, v240
	v_add_f32_e32 v162, v240, v241
	v_mov_b32_e32 v163, v162
	s_nop 0
	s_nop 0
	v_permlane32_swap_b32_e32 v162, v163
	v_max3_f32 v246, v84, v85, v86
	v_max3_f32 v246, v246, v87, v88
	v_max3_f32 v246, v246, v89, v90
	v_max3_f32 v246, v246, v91, v92
	v_max3_f32 v246, v246, v93, v94
	v_max3_f32 v246, v246, v95, v96
	v_max3_f32 v246, v246, v97, v98
	v_max_f32_e32 v246, v246, v99
	v_max3_f32 v248, v68, v69, v70
	s_waitcnt lgkmcnt(2)
	v_mfma_scale_f32_32x32x64_f8f6f4 v[52:67], v[232:239], v[200:207], v[52:67], v188, v188 op_sel_hi:[0,0,0]
	v_max3_f32 v248, v248, v71, v72
	v_max3_f32 v248, v248, v73, v74
	v_max3_f32 v248, v248, v75, v76
	v_max3_f32 v248, v248, v77, v78
	v_max3_f32 v248, v248, v79, v80
	v_max3_f32 v248, v248, v81, v82
	v_max_f32_e32 v248, v248, v83
	v_max_f32_e32 v250, v246, v248
	v_mov_b32_e32 v251, v250
	s_nop 0
	s_nop 0
	v_permlane32_swap_b32_e32 v250, v251
	v_max_f32_e32 v250, v250, v251
	v_cmp_ge_f32_e32 vcc, 0x410a7fad, v250
	s_cmp_eq_u64 vcc, exec
	s_waitcnt lgkmcnt(0)
	v_mfma_scale_f32_32x32x64_f8f6f4 v[36:51], v[232:239], v[208:215], v[36:51], v188, v188 op_sel_hi:[0,0,0]
	ds_read_b128 v[200:203], v197 offset:12288
	ds_read_b128 v[204:207], v198 offset:12288
	ds_read_b128 v[208:211], v197 offset:14336
	ds_read_b128 v[212:215], v198 offset:14336
	s_cselect_b64 s[4:5], -1, 0
	v_max_f32_e32 v250, 0, v250
	v_exp_f32_e64 v155, -v250
	v_fmamk_f32 v2, v250, 0x41000000, v153
	v_cndmask_b32_e64 v164, v155, 1.0, s[4:5]
	v_cndmask_b32_e64 v154, v2, v153, s[4:5]
	v_exp_f32_e32 v165, v84
	v_exp_f32_e32 v169, v85
	v_exp_f32_e32 v2, v86
	v_exp_f32_e32 v155, v87
	v_exp_f32_e32 v166, v88
	v_exp_f32_e32 v170, v89
	v_exp_f32_e32 v156, v90
	s_waitcnt lgkmcnt(2)
	v_mfma_scale_f32_32x32x64_f8f6f4 v[20:35], v[232:239], v[200:207], v[20:35], v188, v188 op_sel_hi:[0,0,0]
	v_exp_f32_e32 v157, v91
	v_exp_f32_e32 v167, v92
	v_exp_f32_e32 v171, v93
	v_exp_f32_e32 v158, v94
	v_exp_f32_e32 v159, v95
	v_exp_f32_e32 v168, v96
	v_exp_f32_e32 v172, v97
	v_exp_f32_e32 v160, v98
	v_exp_f32_e32 v161, v99
	v_exp_f32_e32 v173, v68
	v_exp_f32_e32 v174, v69
	v_exp_f32_e32 v175, v70
	v_exp_f32_e32 v176, v71
	s_waitcnt lgkmcnt(0)
	v_mfma_scale_f32_32x32x64_f8f6f4 v[4:19], v[232:239], v[208:215], v[4:19], v188, v188 op_sel_hi:[0,0,0]
	v_exp_f32_e32 v177, v72
	v_exp_f32_e32 v178, v73
	v_exp_f32_e32 v179, v74
	v_exp_f32_e32 v180, v75
	v_exp_f32_e32 v181, v76
	v_exp_f32_e32 v182, v77
	v_exp_f32_e32 v183, v78
	v_exp_f32_e32 v246, v79
	v_exp_f32_e32 v248, v80
	v_exp_f32_e32 v250, v81
	v_exp_f32_e32 v251, v82
	v_exp_f32_e32 v153, v83
	s_cmp_eq_u64 s[4:5], 0
	s_cbranch_scc0 .Lring_noresc_a1
	s_nop 15
	s_nop 7
	s_and_saveexec_b64 s[8:9], s[6:7]
	ds_write_b32 v184, v164 offset:128
	s_or_b64 exec, exec, s[8:9]
	s_waitcnt lgkmcnt(0)
	v_add_u32_e32 v252, v135, v185
	ds_read_b128 v[212:215], v252 offset:224
	ds_read_b128 v[208:211], v252 offset:192
	ds_read_b128 v[204:207], v252 offset:160
	ds_read_b128 v[200:203], v252 offset:128
	v_mul_f32_e32 v165, v165, v164
	v_mul_f32_e32 v169, v169, v164
	v_mul_f32_e32 v2, v2, v164
	v_mul_f32_e32 v155, v155, v164
	v_mul_f32_e32 v166, v166, v164
	v_mul_f32_e32 v170, v170, v164
	v_mul_f32_e32 v156, v156, v164
	v_mul_f32_e32 v157, v157, v164
	v_mul_f32_e32 v167, v167, v164
	v_mul_f32_e32 v171, v171, v164
	v_mul_f32_e32 v158, v158, v164
	v_mul_f32_e32 v159, v159, v164
	v_mul_f32_e32 v168, v168, v164
	v_mul_f32_e32 v172, v172, v164
	v_mul_f32_e32 v160, v160, v164
	v_mul_f32_e32 v161, v161, v164
	v_mul_f32_e32 v173, v173, v164
	v_mul_f32_e32 v174, v174, v164
	v_mul_f32_e32 v175, v175, v164
	v_mul_f32_e32 v176, v176, v164
	v_mul_f32_e32 v177, v177, v164
	v_mul_f32_e32 v178, v178, v164
	v_mul_f32_e32 v179, v179, v164
	v_mul_f32_e32 v180, v180, v164
	v_mul_f32_e32 v181, v181, v164
	v_mul_f32_e32 v182, v182, v164
	v_mul_f32_e32 v183, v183, v164
	v_mul_f32_e32 v246, v246, v164
	v_mul_f32_e32 v248, v248, v164
	v_mul_f32_e32 v250, v250, v164
	v_mul_f32_e32 v251, v251, v164
	v_mul_f32_e32 v153, v153, v164
	v_mul_f32_e32 v216, 0xbe000000, v154
	v_mov_b32_e32 v217, v216
	v_mov_b32_e32 v218, v216
	v_mov_b32_e32 v219, v216
	v_mov_b32_e32 v220, v216
	v_mov_b32_e32 v221, v216
	v_mov_b32_e32 v222, v216
	v_mov_b32_e32 v223, v216
	v_mov_b32_e32 v224, v216
	v_mov_b32_e32 v225, v216
	v_mov_b32_e32 v226, v216
	v_mov_b32_e32 v227, v216
	v_mov_b32_e32 v228, v216
	v_mov_b32_e32 v229, v216
	v_mov_b32_e32 v230, v216
	v_mov_b32_e32 v231, v216
	s_waitcnt lgkmcnt(0)
	v_pk_mul_f32 v[52:53], v[52:53], v[200:201]
	v_pk_mul_f32 v[54:55], v[54:55], v[202:203]
	v_pk_mul_f32 v[56:57], v[56:57], v[204:205]
	v_pk_mul_f32 v[58:59], v[58:59], v[206:207]
	v_pk_mul_f32 v[60:61], v[60:61], v[208:209]
	v_pk_mul_f32 v[62:63], v[62:63], v[210:211]
	v_pk_mul_f32 v[64:65], v[64:65], v[212:213]
	v_pk_mul_f32 v[66:67], v[66:67], v[214:215]
	v_pk_mul_f32 v[36:37], v[36:37], v[200:201]
	v_pk_mul_f32 v[38:39], v[38:39], v[202:203]
	v_pk_mul_f32 v[40:41], v[40:41], v[204:205]
	v_pk_mul_f32 v[42:43], v[42:43], v[206:207]
	v_pk_mul_f32 v[44:45], v[44:45], v[208:209]
	v_pk_mul_f32 v[46:47], v[46:47], v[210:211]
	v_pk_mul_f32 v[48:49], v[48:49], v[212:213]
	v_pk_mul_f32 v[50:51], v[50:51], v[214:215]
	v_pk_mul_f32 v[20:21], v[20:21], v[200:201]
	v_pk_mul_f32 v[22:23], v[22:23], v[202:203]
	v_pk_mul_f32 v[24:25], v[24:25], v[204:205]
	v_pk_mul_f32 v[26:27], v[26:27], v[206:207]
	v_pk_mul_f32 v[28:29], v[28:29], v[208:209]
	v_pk_mul_f32 v[30:31], v[30:31], v[210:211]
	v_pk_mul_f32 v[32:33], v[32:33], v[212:213]
	v_pk_mul_f32 v[34:35], v[34:35], v[214:215]
	v_pk_mul_f32 v[4:5], v[4:5], v[200:201]
	v_pk_mul_f32 v[6:7], v[6:7], v[202:203]
	v_pk_mul_f32 v[8:9], v[8:9], v[204:205]
	v_pk_mul_f32 v[10:11], v[10:11], v[206:207]
	v_pk_mul_f32 v[12:13], v[12:13], v[208:209]
	v_pk_mul_f32 v[14:15], v[14:15], v[210:211]
	v_pk_mul_f32 v[16:17], v[16:17], v[212:213]
	v_pk_mul_f32 v[18:19], v[18:19], v[214:215]

.Lring_noload_b1:
	ds_read_b128 v[200:203], v192 offset:36864
	ds_read_b128 v[68:71], v192 offset:32768
	ds_read_b128 v[72:75], v193 offset:32768
	ds_read_b128 v[204:207], v193 offset:36864
	v_cvt_pk_fp8_f32 v232, v165, v169
	v_cvt_pk_fp8_f32 v233, v166, v170
	v_cvt_pk_fp8_f32 v234, v167, v171
	v_cvt_pk_fp8_f32 v235, v168, v172
	v_cvt_pk_fp8_f32 v232, v2, v155 op_sel:[0,0,1]
	v_cvt_pk_fp8_f32 v233, v156, v157 op_sel:[0,0,1]
	v_cvt_pk_fp8_f32 v234, v158, v159 op_sel:[0,0,1]
	v_cvt_pk_fp8_f32 v235, v160, v161 op_sel:[0,0,1]
	v_cvt_pk_fp8_f32 v236, v173, v174
	v_cvt_pk_fp8_f32 v237, v177, v178
	v_cvt_pk_fp8_f32 v238, v181, v182
	v_cvt_pk_fp8_f32 v239, v248, v250
	s_waitcnt lgkmcnt(1)
	v_mfma_scale_f32_32x32x64_f8f6f4 v[84:99], v[68:75], v[100:107], v[216:231], v188, v247 op_sel_hi:[0,0,0]
	v_cvt_pk_fp8_f32 v236, v175, v176 op_sel:[0,0,1]
	v_cvt_pk_fp8_f32 v237, v179, v180 op_sel:[0,0,1]
	v_cvt_pk_fp8_f32 v238, v183, v246 op_sel:[0,0,1]
	v_cvt_pk_fp8_f32 v239, v251, v153 op_sel:[0,0,1]
	v_add_f32_e32 v241, v246, v248
	v_add_f32_e32 v240, v165, v169
	v_add_f32_e32 v241, v250, v241
	v_add_f32_e32 v240, v2, v240
	v_add_f32_e32 v241, v251, v241
	v_add_f32_e32 v240, v155, v240
	v_add_f32_e32 v241, v173, v241
	v_add_f32_e32 v240, v166, v240
	s_waitcnt lgkmcnt(0)
	v_mfma_scale_f32_32x32x64_f8f6f4 v[68:83], v[200:207], v[100:107], v[216:231], v188, v247 op_sel_hi:[0,0,0]
	ds_read_b128 v[200:203], v194 offset:36864
	ds_read_b128 v[208:211], v194 offset:32768
	ds_read_b128 v[212:215], v195 offset:32768
	ds_read_b128 v[204:207], v195 offset:36864
	v_add_f32_e32 v241, v174, v241
	v_add_f32_e32 v240, v170, v240
	v_add_f32_e32 v241, v175, v241
	v_add_f32_e32 v240, v156, v240
	v_add_f32_e32 v241, v176, v241
	v_add_f32_e32 v240, v157, v240
	v_add_f32_e32 v241, v177, v241
	v_add_f32_e32 v240, v167, v240
	v_add_f32_e32 v241, v178, v241
	v_add_f32_e32 v240, v171, v240
	v_add_f32_e32 v241, v179, v241
	v_add_f32_e32 v240, v158, v240
	s_waitcnt lgkmcnt(1)
	v_mfma_scale_f32_32x32x64_f8f6f4 v[84:99], v[208:215], v[108:115], v[84:99], v188, v247 op_sel_hi:[0,0,0]
	v_add_f32_e32 v241, v180, v241
	v_add_f32_e32 v240, v159, v240
	v_add_f32_e32 v241, v181, v241
	v_add_f32_e32 v240, v168, v240
	v_add_f32_e32 v241, v182, v241
	v_add_f32_e32 v240, v172, v240
	v_add_f32_e32 v241, v183, v241
	v_add_f32_e32 v240, v160, v240
	v_add_f32_e32 v241, v153, v241
	v_add_f32_e32 v240, v161, v240
	v_add_f32_e32 v181, v240, v241
	v_mov_b32_e32 v182, v181
	s_nop 0
	s_nop 0
	v_permlane32_swap_b32_e32 v181, v182
	s_waitcnt lgkmcnt(0)
	v_mfma_scale_f32_32x32x64_f8f6f4 v[68:83], v[200:207], v[108:115], v[68:83], v188, v247 op_sel_hi:[0,0,0]
	ds_read_b128 v[200:203], v197 offset:24576
	ds_read_b128 v[204:207], v198 offset:24576
	ds_read_b128 v[208:211], v197 offset:26624
	ds_read_b128 v[212:215], v198 offset:26624
	v_max3_f32 v246, v84, v85, v86
	v_max3_f32 v246, v246, v87, v88
	v_max3_f32 v246, v246, v89, v90
	v_max3_f32 v246, v246, v91, v92
	v_max3_f32 v246, v246, v93, v94
	v_max3_f32 v246, v246, v95, v96
	v_max3_f32 v246, v246, v97, v98
	v_max_f32_e32 v246, v246, v99
	s_nop 7
	v_max3_f32 v248, v68, v69, v70
	v_max3_f32 v248, v248, v71, v72
	v_max3_f32 v248, v248, v73, v74
	v_max3_f32 v248, v248, v75, v76
	v_max3_f32 v248, v248, v77, v78
	s_waitcnt lgkmcnt(2)
	v_mfma_scale_f32_32x32x64_f8f6f4 v[52:67], v[232:239], v[200:207], v[52:67], v188, v188 op_sel_hi:[0,0,0]
	v_max3_f32 v248, v248, v79, v80
	v_max3_f32 v248, v248, v81, v82
	v_max_f32_e32 v248, v248, v83
	v_max_f32_e32 v250, v246, v248
	v_mov_b32_e32 v251, v250
	s_nop 0
	s_nop 0
	v_permlane32_swap_b32_e32 v250, v251
	v_max_f32_e32 v250, v250, v251
	v_cmp_ge_f32_e32 vcc, 0x410a7fad, v250
	s_cmp_eq_u64 vcc, exec
	s_cselect_b64 s[4:5], -1, 0
	v_max_f32_e32 v250, 0, v250
	v_exp_f32_e64 v2, -v250
	v_fmamk_f32 v153, v250, 0x41000000, v154
	s_waitcnt lgkmcnt(0)
	v_mfma_scale_f32_32x32x64_f8f6f4 v[36:51], v[232:239], v[208:215], v[36:51], v188, v188 op_sel_hi:[0,0,0]
	ds_read_b128 v[200:203], v197 offset:28672
	ds_read_b128 v[204:207], v198 offset:28672
	ds_read_b128 v[208:211], v197 offset:30720
	ds_read_b128 v[212:215], v198 offset:30720
	v_cndmask_b32_e64 v2, v2, 1.0, s[4:5]
	v_cndmask_b32_e64 v153, v153, v154, s[4:5]
	v_exp_f32_e32 v173, v84
	v_exp_f32_e32 v177, v85
	v_exp_f32_e32 v165, v86
	v_exp_f32_e32 v166, v87
	v_exp_f32_e32 v174, v88
	v_exp_f32_e32 v178, v89
	v_exp_f32_e32 v167, v90
	v_exp_f32_e32 v168, v91
	v_exp_f32_e32 v175, v92
	v_exp_f32_e32 v179, v93
	v_exp_f32_e32 v169, v94
	s_waitcnt lgkmcnt(2)
	v_mfma_scale_f32_32x32x64_f8f6f4 v[20:35], v[232:239], v[200:207], v[20:35], v188, v188 op_sel_hi:[0,0,0]
	v_exp_f32_e32 v170, v95
	v_exp_f32_e32 v176, v96
	v_exp_f32_e32 v180, v97
	v_exp_f32_e32 v171, v98
	v_exp_f32_e32 v172, v99
	v_exp_f32_e32 v154, v68
	v_exp_f32_e32 v155, v69
	v_exp_f32_e32 v130, v70
	v_exp_f32_e32 v131, v71
	v_exp_f32_e32 v128, v72
	v_exp_f32_e32 v129, v73
	v_exp_f32_e32 v126, v74
	v_exp_f32_e32 v127, v75
	s_waitcnt lgkmcnt(0)
	v_mfma_scale_f32_32x32x64_f8f6f4 v[4:19], v[232:239], v[208:215], v[4:19], v188, v188 op_sel_hi:[0,0,0]
	v_exp_f32_e32 v124, v76
	v_exp_f32_e32 v125, v77
	v_exp_f32_e32 v160, v78
	v_exp_f32_e32 v161, v79
	v_exp_f32_e32 v158, v80
	v_exp_f32_e32 v159, v81
	v_exp_f32_e32 v156, v82
	v_exp_f32_e32 v157, v83
	v_add_f32_e32 v249, v162, v163
	v_fmac_f32_e32 v249, v147, v145
	v_add_f32_e32 v145, v181, v182
	v_fmac_f32_e32 v145, v249, v164
	s_cmp_eq_u64 s[4:5], 0
	s_cbranch_scc0 .Lring_noresc_b1
	s_nop 15
	s_nop 7
	s_and_saveexec_b64 s[10:11], s[6:7]
	ds_write_b32 v184, v2 offset:128
	s_or_b64 exec, exec, s[10:11]
	s_waitcnt lgkmcnt(0)
	v_add_u32_e32 v252, v135, v185
	ds_read_b128 v[212:215], v252 offset:224
	ds_read_b128 v[208:211], v252 offset:192
	ds_read_b128 v[204:207], v252 offset:160
	ds_read_b128 v[200:203], v252 offset:128
	v_mul_f32_e32 v173, v173, v2
	v_mul_f32_e32 v177, v177, v2
	v_mul_f32_e32 v165, v165, v2
	v_mul_f32_e32 v166, v166, v2
	v_mul_f32_e32 v174, v174, v2
	v_mul_f32_e32 v178, v178, v2
	v_mul_f32_e32 v167, v167, v2
	v_mul_f32_e32 v168, v168, v2
	v_mul_f32_e32 v175, v175, v2
	v_mul_f32_e32 v179, v179, v2
	v_mul_f32_e32 v169, v169, v2
	v_mul_f32_e32 v170, v170, v2
	v_mul_f32_e32 v176, v176, v2
	v_mul_f32_e32 v180, v180, v2
	v_mul_f32_e32 v171, v171, v2
	v_mul_f32_e32 v172, v172, v2
	v_mul_f32_e32 v154, v154, v2
	v_mul_f32_e32 v155, v155, v2
	v_mul_f32_e32 v130, v130, v2
	v_mul_f32_e32 v131, v131, v2
	v_mul_f32_e32 v128, v128, v2
	v_mul_f32_e32 v129, v129, v2
	v_mul_f32_e32 v126, v126, v2
	v_mul_f32_e32 v127, v127, v2
	v_mul_f32_e32 v124, v124, v2
	v_mul_f32_e32 v125, v125, v2
	v_mul_f32_e32 v160, v160, v2
	v_mul_f32_e32 v161, v161, v2
	v_mul_f32_e32 v158, v158, v2
	v_mul_f32_e32 v159, v159, v2
	v_mul_f32_e32 v156, v156, v2
	v_mul_f32_e32 v157, v157, v2
	v_mul_f32_e32 v216, 0xbe000000, v153
	v_mov_b32_e32 v217, v216
	v_mov_b32_e32 v218, v216
	v_mov_b32_e32 v219, v216
	v_mov_b32_e32 v220, v216
	v_mov_b32_e32 v221, v216
	v_mov_b32_e32 v222, v216
	v_mov_b32_e32 v223, v216
	v_mov_b32_e32 v224, v216
	v_mov_b32_e32 v225, v216
	v_mov_b32_e32 v226, v216
	v_mov_b32_e32 v227, v216
	v_mov_b32_e32 v228, v216
	v_mov_b32_e32 v229, v216
	v_mov_b32_e32 v230, v216
	v_mov_b32_e32 v231, v216
	s_waitcnt lgkmcnt(0)
	v_pk_mul_f32 v[52:53], v[52:53], v[200:201]
	v_pk_mul_f32 v[54:55], v[54:55], v[202:203]
	v_pk_mul_f32 v[56:57], v[56:57], v[204:205]
	v_pk_mul_f32 v[58:59], v[58:59], v[206:207]
	v_pk_mul_f32 v[60:61], v[60:61], v[208:209]
	v_pk_mul_f32 v[62:63], v[62:63], v[210:211]
	v_pk_mul_f32 v[64:65], v[64:65], v[212:213]
	v_pk_mul_f32 v[66:67], v[66:67], v[214:215]
	v_pk_mul_f32 v[36:37], v[36:37], v[200:201]
	v_pk_mul_f32 v[38:39], v[38:39], v[202:203]
	v_pk_mul_f32 v[40:41], v[40:41], v[204:205]
	v_pk_mul_f32 v[42:43], v[42:43], v[206:207]
	v_pk_mul_f32 v[44:45], v[44:45], v[208:209]
	v_pk_mul_f32 v[46:47], v[46:47], v[210:211]
	v_pk_mul_f32 v[48:49], v[48:49], v[212:213]
	v_pk_mul_f32 v[50:51], v[50:51], v[214:215]
	v_pk_mul_f32 v[20:21], v[20:21], v[200:201]
	v_pk_mul_f32 v[22:23], v[22:23], v[202:203]
	v_pk_mul_f32 v[24:25], v[24:25], v[204:205]
	v_pk_mul_f32 v[26:27], v[26:27], v[206:207]
	v_pk_mul_f32 v[28:29], v[28:29], v[208:209]
	v_pk_mul_f32 v[30:31], v[30:31], v[210:211]
	v_pk_mul_f32 v[32:33], v[32:33], v[212:213]
	v_pk_mul_f32 v[34:35], v[34:35], v[214:215]
	v_pk_mul_f32 v[4:5], v[4:5], v[200:201]
	v_pk_mul_f32 v[6:7], v[6:7], v[202:203]
	v_pk_mul_f32 v[8:9], v[8:9], v[204:205]
	v_pk_mul_f32 v[10:11], v[10:11], v[206:207]
	v_pk_mul_f32 v[12:13], v[12:13], v[208:209]
	v_pk_mul_f32 v[14:15], v[14:15], v[210:211]
	v_pk_mul_f32 v[16:17], v[16:17], v[212:213]
	v_pk_mul_f32 v[18:19], v[18:19], v[214:215]

.LBB0_421:
	ds_read_b128 v[116:119], v192 offset:61440
	ds_read_b128 v[68:71], v192 offset:57344
	ds_read_b128 v[72:75], v193 offset:57344
	ds_read_b128 v[120:123], v193 offset:61440
	s_waitcnt lgkmcnt(1)
	v_mfma_scale_f32_32x32x64_f8f6f4 v[84:99], v[68:75], v[100:107], 0, v188, v188 op_sel_hi:[0,0,0]
	s_waitcnt lgkmcnt(0)
	v_mfma_scale_f32_32x32x64_f8f6f4 v[68:83], v[116:123], v[100:107], 0, v188, v188 op_sel_hi:[0,0,0]
	ds_read_b128 v[100:103], v194 offset:61440
	ds_read_b128 v[116:119], v194 offset:57344
	ds_read_b128 v[120:123], v195 offset:57344
	ds_read_b128 v[104:107], v195 offset:61440
	s_waitcnt lgkmcnt(1)
	v_mfma_scale_f32_32x32x64_f8f6f4 v[84:99], v[116:123], v[108:115], v[84:99], v188, v188 op_sel_hi:[0,0,0]
	s_waitcnt lgkmcnt(0)
	v_mfma_scale_f32_32x32x64_f8f6f4 v[68:83], v[100:107], v[108:115], v[68:83], v188, v188 op_sel_hi:[0,0,0]
	v_add_f32_e32 v100, 0, v173
	v_add_f32_e32 v100, v177, v100
	v_add_f32_e32 v100, v165, v100
	v_add_f32_e32 v100, v166, v100
	v_add_f32_e32 v100, v174, v100
	v_add_f32_e32 v100, v178, v100
	v_add_f32_e32 v100, v167, v100
	v_add_f32_e32 v100, v168, v100
	v_add_f32_e32 v100, v175, v100
	v_add_f32_e32 v100, v179, v100
	v_add_f32_e32 v100, v169, v100
	v_add_f32_e32 v100, v170, v100
	v_mov_b32_e32 v101, v154
	v_add_f32_e32 v100, v176, v100
	v_mov_b32_e32 v107, v155
	v_add_f32_e32 v100, v180, v100
	v_mov_b32_e32 v110, v130
	v_add_f32_e32 v100, v171, v100
	v_mov_b32_e32 v111, v131
	v_add_f32_e32 v100, v172, v100
	v_mov_b32_e32 v108, v128
	v_add_f32_e32 v100, v101, v100
	v_mov_b32_e32 v109, v129
	v_add_f32_e32 v100, v107, v100
	v_mov_b32_e32 v112, v126
	v_add_f32_e32 v100, v110, v100
	v_mov_b32_e32 v113, v127
	v_add_f32_e32 v100, v111, v100
	v_mov_b32_e32 v114, v124
	v_add_f32_e32 v100, v108, v100
	v_mov_b32_e32 v115, v125
	v_add_f32_e32 v100, v109, v100
	v_mov_b32_e32 v116, v160
	v_add_f32_e32 v100, v112, v100
	v_mov_b32_e32 v117, v161
	v_add_f32_e32 v100, v113, v100
	v_mov_b32_e32 v118, v158
	v_add_f32_e32 v100, v114, v100
	v_mov_b32_e32 v119, v159
	v_add_f32_e32 v100, v115, v100
	v_mov_b32_e32 v102, v3
	v_mov_b32_e32 v103, v3
	v_mov_b32_e32 v120, v156
	v_add_f32_e32 v100, v116, v100
	v_cvt_pk_fp8_f32 v102, v173, v177
	v_cvt_pk_fp8_f32 v103, v174, v178
	v_mov_b32_e32 v121, v157
	v_add_f32_e32 v100, v117, v100
	v_mov_b32_e32 v106, v3
	v_add_f32_e32 v100, v118, v100
	v_cvt_pk_fp8_f32 v106, v101, v107
	v_mov_b32_e32 v107, v3
	v_add_f32_e32 v100, v119, v100
	v_mov_b32_e32 v104, v3
	v_mov_b32_e32 v105, v3
	v_cvt_pk_fp8_f32 v107, v108, v109
	v_mov_b32_e32 v108, v3
	v_mov_b32_e32 v109, v3
	v_add_f32_e32 v100, v120, v100
	v_cvt_pk_fp8_f32 v104, v175, v179
	v_cvt_pk_fp8_f32 v105, v176, v180
	v_cvt_pk_fp8_f32 v102, v165, v166 op_sel:[0,0,1]
	v_cvt_pk_fp8_f32 v103, v167, v168 op_sel:[0,0,1]
	v_cvt_pk_fp8_f32 v108, v114, v115
	v_cvt_pk_fp8_f32 v109, v118, v119
	v_add_f32_e32 v100, v121, v100
	v_mov_b32_e32 v101, v100
	s_nop 1
	v_permlane32_swap_b32_e32 v100, v101
	s_nop 15
	s_nop 15
	v_cvt_pk_fp8_f32 v104, v169, v170 op_sel:[0,0,1]
	v_cvt_pk_fp8_f32 v105, v171, v172 op_sel:[0,0,1]
	v_cvt_pk_fp8_f32 v106, v110, v111 op_sel:[0,0,1]
	v_cvt_pk_fp8_f32 v107, v112, v113 op_sel:[0,0,1]
	v_cvt_pk_fp8_f32 v108, v116, v117 op_sel:[0,0,1]
	v_cvt_pk_fp8_f32 v109, v120, v121 op_sel:[0,0,1]
	ds_read_b128 v[110:113], v197 offset:8192
	ds_read_b128 v[118:121], v197 offset:10240
	ds_read_b128 v[114:117], v198 offset:8192
	ds_read_b128 v[122:125], v198 offset:10240
	ds_read_b128 v[154:157], v197 offset:12288
	ds_read_b128 v[162:165], v197 offset:14336
	ds_read_b128 v[158:161], v198 offset:12288
	ds_read_b128 v[166:169], v198 offset:14336
	s_waitcnt lgkmcnt(5)
	v_mfma_scale_f32_32x32x64_f8f6f4 v[52:67], v[102:109], v[110:117], v[52:67], v188, v188 op_sel_hi:[0,0,0]
	s_waitcnt lgkmcnt(4)
	v_mfma_scale_f32_32x32x64_f8f6f4 v[36:51], v[102:109], v[118:125], v[36:51], v188, v188 op_sel_hi:[0,0,0]
	s_waitcnt lgkmcnt(1)
	v_mfma_scale_f32_32x32x64_f8f6f4 v[20:35], v[102:109], v[154:161], v[20:35], v188, v188 op_sel_hi:[0,0,0]
	s_waitcnt lgkmcnt(0)
	v_mfma_scale_f32_32x32x64_f8f6f4 v[4:19], v[102:109], v[162:169], v[4:19], v188, v188 op_sel_hi:[0,0,0]
	v_max_f32_e32 v102, v85, v85
	v_max_f32_e32 v103, v84, v84
	v_max_f32_e32 v102, v103, v102
	v_max3_f32 v102, v102, v86, v87
	v_max3_f32 v102, v102, v88, v89
	v_max3_f32 v102, v102, v90, v91
	v_max3_f32 v102, v102, v92, v93
	v_max3_f32 v102, v102, v94, v95
	v_max3_f32 v102, v102, v96, v97
	v_max3_f32 v102, v102, v98, v99
	v_max3_f32 v102, v102, v68, v69
	v_max3_f32 v102, v102, v70, v71
	v_max3_f32 v102, v102, v72, v73
	v_max3_f32 v102, v102, v74, v75
	v_max3_f32 v102, v102, v76, v77
	v_max3_f32 v102, v102, v78, v79
	v_max3_f32 v102, v102, v80, v81
	v_max3_f32 v102, v102, v82, v83
	v_mov_b32_e32 v103, v102
	s_nop 1
	v_permlane32_swap_b32_e32 v102, v103
	v_max_f32_e32 v103, v103, v103
	v_max_f32_e32 v102, v102, v102
	v_max_f32_e32 v102, v102, v103
	v_max_f32_e32 v103, v153, v153
	v_max_f32_e32 v103, v103, v102
	v_sub_f32_e32 v104, v102, v153
	v_sub_f32_e32 v102, v153, v103
	v_mul_f32_e32 v102, 0x3e000000, v102
	v_exp_f32_e32 v102, v102
	v_cmp_ge_f32_e32 vcc, s55, v104
	s_cmp_eq_u64 vcc, exec
	s_cselect_b64 s[4:5], -1, 0
	v_cndmask_b32_e64 v102, v102, 1.0, s[4:5]
	v_cmp_gt_f32_e32 vcc, 1.0, v102
	s_nop 15
	s_nop 15
	s_barrier
	s_cbranch_vccz .LBB0_425
	s_and_saveexec_b64 s[8:9], s[6:7]
	ds_write_b32 v184, v102 offset:128
	s_or_b64 exec, exec, s[8:9]
	s_waitcnt lgkmcnt(0)
	v_add_u32_e32 v116, v135, v185
	ds_read_b128 v[104:107], v116 offset:224
	ds_read_b128 v[108:111], v116 offset:192
	ds_read_b128 v[112:115], v116 offset:160
	ds_read_b128 v[116:119], v116 offset:128
	s_waitcnt lgkmcnt(3)
	v_pk_mul_f32 v[64:65], v[64:65], v[104:105]
	s_waitcnt lgkmcnt(2)
	v_pk_mul_f32 v[60:61], v[60:61], v[108:109]
	s_waitcnt lgkmcnt(1)
	v_pk_mul_f32 v[56:57], v[56:57], v[112:113]
	v_pk_mul_f32 v[66:67], v[66:67], v[106:107]
	v_pk_mul_f32 v[62:63], v[62:63], v[110:111]
	v_pk_mul_f32 v[58:59], v[58:59], v[114:115]
	s_waitcnt lgkmcnt(0)
	v_pk_mul_f32 v[54:55], v[54:55], v[118:119]
	v_pk_mul_f32 v[52:53], v[52:53], v[116:117]
	v_pk_mul_f32 v[48:49], v[48:49], v[104:105]
	v_pk_mul_f32 v[44:45], v[44:45], v[108:109]
	v_pk_mul_f32 v[40:41], v[40:41], v[112:113]
	v_pk_mul_f32 v[50:51], v[50:51], v[106:107]
	v_pk_mul_f32 v[46:47], v[46:47], v[110:111]
	v_pk_mul_f32 v[42:43], v[42:43], v[114:115]
	v_pk_mul_f32 v[38:39], v[38:39], v[118:119]
	v_pk_mul_f32 v[36:37], v[36:37], v[116:117]
	v_pk_mul_f32 v[32:33], v[32:33], v[104:105]
	v_pk_mul_f32 v[28:29], v[28:29], v[108:109]
	v_pk_mul_f32 v[24:25], v[24:25], v[112:113]
	v_pk_mul_f32 v[34:35], v[34:35], v[106:107]
	v_pk_mul_f32 v[30:31], v[30:31], v[110:111]
	v_pk_mul_f32 v[26:27], v[26:27], v[114:115]
	v_pk_mul_f32 v[22:23], v[22:23], v[118:119]
	v_pk_mul_f32 v[20:21], v[20:21], v[116:117]
	v_pk_mul_f32 v[16:17], v[16:17], v[104:105]
	v_pk_mul_f32 v[12:13], v[12:13], v[108:109]
	v_pk_mul_f32 v[8:9], v[8:9], v[112:113]
	v_pk_mul_f32 v[18:19], v[18:19], v[106:107]
	v_pk_mul_f32 v[14:15], v[14:15], v[110:111]
	v_pk_mul_f32 v[10:11], v[10:11], v[114:115]
	v_pk_mul_f32 v[6:7], v[6:7], v[118:119]
	v_pk_mul_f32 v[4:5], v[4:5], v[116:117]
.LBB0_425:
	v_cndmask_b32_e64 v103, v103, v153, s[4:5]
	v_mul_f32_e32 v103, 0xbe000000, v103
	v_fmamk_f32 v84, v84, 0x3e000000, v103
	v_fmamk_f32 v85, v85, 0x3e000000, v103
	v_fmamk_f32 v112, v96, 0x3e000000, v103
	v_fmamk_f32 v96, v77, 0x3e000000, v103
	v_exp_f32_e32 v77, v84
	v_fmamk_f32 v86, v86, 0x3e000000, v103
	v_exp_f32_e32 v84, v85
	v_fmamk_f32 v87, v87, 0x3e000000, v103
	v_fmamk_f32 v104, v88, 0x3e000000, v103
	v_fmamk_f32 v88, v69, 0x3e000000, v103
	v_exp_f32_e32 v69, v86
	v_fmamk_f32 v105, v89, 0x3e000000, v103
	v_fmamk_f32 v68, v68, 0x3e000000, v103
	v_fmamk_f32 v89, v70, 0x3e000000, v103
	v_exp_f32_e32 v70, v87
	v_fmamk_f32 v113, v97, 0x3e000000, v103
	v_fmamk_f32 v97, v78, 0x3e000000, v103
	v_exp_f32_e32 v78, v104
	v_exp_f32_e32 v104, v68
	v_add_f32_e32 v68, 0, v77
	v_fmamk_f32 v106, v90, 0x3e000000, v103
	v_exp_f32_e32 v85, v105
	v_add_f32_e32 v68, v84, v68
	v_fmamk_f32 v107, v91, 0x3e000000, v103
	v_fmamk_f32 v90, v71, 0x3e000000, v103
	v_exp_f32_e32 v71, v106
	v_add_f32_e32 v68, v69, v68
	v_fmamk_f32 v108, v92, 0x3e000000, v103
	v_fmamk_f32 v91, v72, 0x3e000000, v103
	v_exp_f32_e32 v72, v107
	v_add_f32_e32 v68, v70, v68
	v_fmamk_f32 v109, v93, 0x3e000000, v103
	v_fmamk_f32 v114, v98, 0x3e000000, v103
	v_fmamk_f32 v98, v79, 0x3e000000, v103
	v_exp_f32_e32 v79, v108
	v_add_f32_e32 v68, v78, v68
	v_fmamk_f32 v110, v94, 0x3e000000, v103
	v_exp_f32_e32 v86, v109
	v_add_f32_e32 v68, v85, v68
	v_fmamk_f32 v111, v95, 0x3e000000, v103
	v_fmamk_f32 v92, v73, 0x3e000000, v103
	v_exp_f32_e32 v73, v110
	v_add_f32_e32 v68, v71, v68
	v_fmamk_f32 v93, v74, 0x3e000000, v103
	v_exp_f32_e32 v74, v111
	v_add_f32_e32 v68, v72, v68
	v_fmamk_f32 v115, v99, 0x3e000000, v103
	v_fmamk_f32 v99, v80, 0x3e000000, v103
	v_exp_f32_e32 v80, v112
	v_add_f32_e32 v68, v79, v68
	v_exp_f32_e32 v87, v113
	v_add_f32_e32 v68, v86, v68
	v_fmamk_f32 v94, v75, 0x3e000000, v103
	v_exp_f32_e32 v75, v114
	v_add_f32_e32 v68, v73, v68
	v_fmamk_f32 v95, v76, 0x3e000000, v103
	v_exp_f32_e32 v76, v115
	v_add_f32_e32 v68, v74, v68
	v_add_f32_e32 v68, v80, v68
	v_exp_f32_e32 v88, v88
	v_add_f32_e32 v68, v87, v68
	v_exp_f32_e32 v105, v89
	v_add_f32_e32 v68, v75, v68
	v_exp_f32_e32 v90, v90
	v_add_f32_e32 v68, v76, v68
	v_exp_f32_e32 v89, v91
	v_add_f32_e32 v68, v104, v68
	v_exp_f32_e32 v91, v92
	v_add_f32_e32 v68, v88, v68
	v_exp_f32_e32 v92, v93
	v_add_f32_e32 v68, v105, v68
	v_exp_f32_e32 v93, v94
	v_add_f32_e32 v68, v90, v68
	v_exp_f32_e32 v94, v95
	v_add_f32_e32 v68, v89, v68
	v_exp_f32_e32 v95, v96
	v_add_f32_e32 v68, v91, v68
	v_exp_f32_e32 v96, v97
	v_add_f32_e32 v68, v92, v68
	v_exp_f32_e32 v97, v98
	v_add_f32_e32 v68, v93, v68
	v_fmamk_f32 v81, v81, 0x3e000000, v103
	v_exp_f32_e32 v98, v99
	v_add_f32_e32 v68, v94, v68
	v_fmamk_f32 v82, v82, 0x3e000000, v103
	v_exp_f32_e32 v81, v81
	v_add_f32_e32 v68, v95, v68
	v_fmac_f32_e32 v103, 0x3e000000, v83
	v_exp_f32_e32 v99, v82
	v_add_f32_e32 v68, v96, v68
	v_mov_b32_e32 v82, v3
	v_mov_b32_e32 v83, v3
	v_exp_f32_e32 v103, v103
	v_add_f32_e32 v68, v97, v68
	v_cvt_pk_fp8_f32 v82, v77, v84
	v_cvt_pk_fp8_f32 v83, v78, v85
	v_mov_b32_e32 v84, v3
	v_mov_b32_e32 v85, v3
	v_add_f32_e32 v68, v98, v68
	v_cvt_pk_fp8_f32 v84, v79, v86
	v_cvt_pk_fp8_f32 v85, v80, v87
	v_mov_b32_e32 v86, v3
	v_mov_b32_e32 v87, v3
	v_add_f32_e32 v68, v81, v68
	v_cvt_pk_fp8_f32 v86, v104, v88
	v_cvt_pk_fp8_f32 v87, v89, v91
	v_mov_b32_e32 v88, v3
	v_mov_b32_e32 v89, v3
	v_add_f32_e32 v68, v99, v68
	v_cvt_pk_fp8_f32 v88, v94, v95
	v_cvt_pk_fp8_f32 v89, v98, v81
	v_add_f32_e32 v68, v103, v68
	v_cvt_pk_fp8_f32 v82, v69, v70 op_sel:[0,0,1]
	v_mov_b32_e32 v69, v68
	s_nop 1
	v_permlane32_swap_b32_e32 v68, v69
	v_cvt_pk_fp8_f32 v83, v71, v72 op_sel:[0,0,1]
	v_cvt_pk_fp8_f32 v84, v73, v74 op_sel:[0,0,1]
	v_cvt_pk_fp8_f32 v85, v75, v76 op_sel:[0,0,1]
	v_cvt_pk_fp8_f32 v86, v105, v90 op_sel:[0,0,1]
	v_cvt_pk_fp8_f32 v87, v92, v93 op_sel:[0,0,1]
	v_cvt_pk_fp8_f32 v88, v96, v97 op_sel:[0,0,1]
	v_cvt_pk_fp8_f32 v89, v99, v103 op_sel:[0,0,1]
	ds_read_b128 v[70:73], v197 offset:24576
	ds_read_b128 v[90:93], v197 offset:26624
	ds_read_b128 v[74:77], v198 offset:24576
	ds_read_b128 v[94:97], v198 offset:26624
	ds_read_b128 v[104:107], v197 offset:28672
	ds_read_b128 v[112:115], v197 offset:30720
	ds_read_b128 v[108:111], v198 offset:28672
	ds_read_b128 v[116:119], v198 offset:30720
	s_waitcnt lgkmcnt(5)
	v_mfma_scale_f32_32x32x64_f8f6f4 v[52:67], v[82:89], v[70:77], v[52:67], v188, v188 op_sel_hi:[0,0,0]
	s_waitcnt lgkmcnt(4)
	v_mfma_scale_f32_32x32x64_f8f6f4 v[36:51], v[82:89], v[90:97], v[36:51], v188, v188 op_sel_hi:[0,0,0]
	s_waitcnt lgkmcnt(1)
	v_mfma_scale_f32_32x32x64_f8f6f4 v[20:35], v[82:89], v[104:111], v[20:35], v188, v188 op_sel_hi:[0,0,0]
	s_waitcnt lgkmcnt(0)
	v_mfma_scale_f32_32x32x64_f8f6f4 v[4:19], v[82:89], v[112:119], v[4:19], v188, v188 op_sel_hi:[0,0,0]
	s_nop 0
	s_nop 15
	s_nop 15
	s_and_saveexec_b64 s[4:5], s[6:7]
	s_cbranch_execz .LBB0_386
	v_add_f32_e32 v70, v100, v101
	v_fmac_f32_e32 v70, v145, v2
	v_add_f32_e32 v2, v68, v69
	v_fmac_f32_e32 v2, v70, v102
	ds_write_b32 v184, v2
	s_branch .LBB0_386
